# attention output rows stored as dwordx4 after a v_permlane16_swap row exchange (half the store instructions) (on top of v70)
# speedup vs baseline: 1.0139x; 1.0122x over previous
.LBB0_1396:
	s_or_b64 exec, exec, s[6:7]
	s_add_u32 s14, s12, 0x18000000
	s_addc_u32 s15, s13, 0
	s_add_u32 s16, s12, 0x2a000000
	s_addc_u32 s17, s13, 0
	s_add_u32 s30, s12, 0x22000000
	s_addc_u32 s31, s13, 0
	v_readfirstlane_b32 s33, v0
	v_and_b32_e32 v2, 15, v242
	v_lshrrev_b32_e32 v3, 4, v242
	s_lshr_b32 s33, s33, 6
	v_lshrrev_b32_e32 v232, 1, v0
	v_and_b32_e32 v233, 1, v0
	v_mul_u32_u24_e32 v4, 0x90, v232
	v_lshl_add_u32 v4, v233, 6, v4
	v_mul_u32_u24_e32 v6, 0x1400, v232
	v_lshl_add_u32 v6, v233, 6, v6
	v_lshlrev_b32_e32 v234, 7, v233
	v_add_u32_e32 v19, 0x15400, v234
	v_lshrrev_b32_e32 v232, 3, v0
	v_and_b32_e32 v233, 7, v0
	v_mul_u32_u24_e32 v5, 0x210, v232
	v_lshl_add_u32 v5, v233, 4, v5
	v_add_u32_e32 v5, 0x9000, v5
	v_lshlrev_b32_e32 v7, 15, v232
	v_lshl_add_u32 v7, v233, 4, v7
	v_mul_u32_u24_e32 v8, 0x1400, v2
	v_lshl_add_u32 v8, v3, 4, v8
	v_lshlrev_b32_e32 v9, 12, v2
	v_lshl_add_u32 v9, v3, 3, v9
	v_lshrrev_b32_e32 v232, 1, v3
	v_and_b32_e32 v233, 1, v3
	v_lshlrev_b32_e32 v91, 12, v2
	v_lshl_add_u32 v91, v232, 4, v91
	v_lshl_add_u32 v91, v233, 5, v91
	v_mul_u32_u24_e32 v10, 0x90, v2
	v_lshl_add_u32 v10, v3, 4, v10
	v_mul_u32_u24_e32 v11, 0x210, v2
	v_bfe_u32 v232, v2, 3, 1
	v_xor_b32_e32 v232, v232, v3
	v_lshl_add_u32 v11, v232, 3, v11
	v_add_u32_e32 v11, 0x9000, v11
	v_add_u32_e32 v12, 0x2100, v11
	v_add_u32_e32 v13, 0x4200, v11
	v_add_u32_e32 v14, 0x6300, v11
	v_xor_b32_e32 v15, 16, v242
	v_lshlrev_b32_e32 v15, 2, v15
	v_xor_b32_e32 v16, 32, v242
	v_lshlrev_b32_e32 v16, 2, v16
	v_xor_b32_e32 v17, 1, v242
	v_lshlrev_b32_e32 v17, 2, v17
	v_lshlrev_b32_e32 v232, 2, v3
	v_sub_u32_e32 v18, v2, v232
	v_add_u32_e32 v18, 0x80, v18
	v_mov_b32_e32 v89, 0xff800000
	v_mov_b32_e32 v90, 0
	v_mov_b32_e32 v144, 0
	v_mov_b32_e32 v145, 0
	s_mov_b32 s34, s96
	s_mov_b32 s55, -1
	s_waitcnt lgkmcnt(0)
	s_barrier
	s_cmpk_gt_u32 s34, 0x3ff
	s_cbranch_scc1 .Lat_done
	s_and_b32 s3, s34, 3
	s_bfe_u32 s4, s34, 0x70002
	s_lshr_b32 s5, s34, 9
	s_lshl_b32 s6, s5, 14
	s_lshl_b32 s7, s4, 7
	s_add_i32 s6, s6, s7
	s_sub_i32 s6, s6, 0x80
	s_mul_i32 s7, s6, 0x1400
	s_ashr_i32 s9, s7, 31
	s_add_u32 s40, s14, s7
	s_addc_u32 s41, s15, s9
	s_lshl_b32 s7, s3, 7
	s_add_u32 s40, s40, s7
	s_addc_u32 s41, s41, 0
	s_lshl_b32 s6, s5, 2
	s_add_i32 s6, s6, s3
	s_lshl_b32 s6, s6, 21
	s_lshl_b32 s7, s4, 8
	s_sub_i32 s7, s7, 0x100
	s_add_i32 s6, s6, s7
	s_ashr_i32 s7, s6, 31
	s_add_u32 s42, s16, s6
	s_addc_u32 s43, s17, s7
	global_load_dwordx4 v[92:95], v6, s[40:41] offset:0
	global_load_dwordx4 v[96:99], v6, s[40:41] offset:16
	global_load_dwordx4 v[100:103], v6, s[40:41] offset:32
	global_load_dwordx4 v[104:107], v6, s[40:41] offset:48
	global_load_dwordx4 v[112:115], v7, s[42:43] offset:0
	global_load_dwordx4 v[120:123], v7, s[42:43] offset:128
	global_load_dwordx4 v[128:131], v7, s[42:43] offset:256
	global_load_dwordx4 v[136:139], v7, s[42:43] offset:384

.Lat_m0:
	s_nop 0
	v_pk_add_f32 v[232:233], v[108:109], v[110:111]
	v_pk_add_f32 v[234:235], v[112:113], v[114:115]
	v_pk_add_f32 v[226:227], v[148:149], v[150:151]
	v_pk_add_f32 v[228:229], v[152:153], v[154:155]
	v_pk_add_f32 v[232:233], v[232:233], v[116:117]
	v_pk_add_f32 v[234:235], v[234:235], v[118:119]
	v_pk_add_f32 v[226:227], v[226:227], v[156:157]
	v_pk_add_f32 v[228:229], v[228:229], v[158:159]
	v_pk_add_f32 v[232:233], v[232:233], v[120:121]
	v_pk_add_f32 v[234:235], v[234:235], v[122:123]
	v_pk_add_f32 v[226:227], v[226:227], v[160:161]
	v_pk_add_f32 v[228:229], v[228:229], v[162:163]
	v_pk_add_f32 v[232:233], v[232:233], v[124:125]
	v_pk_add_f32 v[234:235], v[234:235], v[126:127]
	v_pk_add_f32 v[226:227], v[226:227], v[164:165]
	v_pk_add_f32 v[228:229], v[228:229], v[166:167]
	v_pk_add_f32 v[232:233], v[232:233], v[128:129]
	v_pk_add_f32 v[234:235], v[234:235], v[130:131]
	v_pk_add_f32 v[226:227], v[226:227], v[168:169]
	v_pk_add_f32 v[228:229], v[228:229], v[170:171]
	v_pk_add_f32 v[232:233], v[232:233], v[132:133]
	v_pk_add_f32 v[234:235], v[234:235], v[134:135]
	v_pk_add_f32 v[226:227], v[226:227], v[172:173]
	v_pk_add_f32 v[228:229], v[228:229], v[174:175]
	v_pk_add_f32 v[232:233], v[232:233], v[136:137]
	v_pk_add_f32 v[234:235], v[234:235], v[138:139]
	v_pk_add_f32 v[226:227], v[226:227], v[176:177]
	v_pk_add_f32 v[228:229], v[228:229], v[178:179]
	v_pk_add_f32 v[232:233], v[232:233], v[140:141]
	v_pk_add_f32 v[234:235], v[234:235], v[142:143]
	v_pk_add_f32 v[226:227], v[226:227], v[180:181]
	v_pk_add_f32 v[228:229], v[228:229], v[182:183]
	v_pk_add_f32 v[232:233], v[232:233], v[234:235]
	v_pk_add_f32 v[226:227], v[226:227], v[228:229]
	v_add_f32_e32 v232, v232, v233
	v_add_f32_e32 v226, v226, v227
	v_cvt_pk_bf16_f32 v108, v108, v109
	v_cvt_pk_bf16_f32 v109, v110, v111
	v_cvt_pk_bf16_f32 v110, v112, v113
	v_cvt_pk_bf16_f32 v111, v114, v115
	v_cvt_pk_bf16_f32 v146, v148, v149
	v_cvt_pk_bf16_f32 v147, v150, v151
	v_cvt_pk_bf16_f32 v116, v116, v117
	v_cvt_pk_bf16_f32 v117, v118, v119
	v_cvt_pk_bf16_f32 v118, v120, v121
	v_cvt_pk_bf16_f32 v119, v122, v123
	v_cvt_pk_bf16_f32 v152, v152, v153
	v_cvt_pk_bf16_f32 v153, v154, v155
	v_cvt_pk_bf16_f32 v154, v156, v157
	v_cvt_pk_bf16_f32 v155, v158, v159
	v_cvt_pk_bf16_f32 v124, v124, v125
	v_cvt_pk_bf16_f32 v125, v126, v127
	v_cvt_pk_bf16_f32 v126, v128, v129
	v_cvt_pk_bf16_f32 v127, v130, v131
	v_cvt_pk_bf16_f32 v160, v160, v161
	v_cvt_pk_bf16_f32 v161, v162, v163
	v_cvt_pk_bf16_f32 v162, v164, v165
	v_cvt_pk_bf16_f32 v163, v166, v167
	v_cvt_pk_bf16_f32 v132, v132, v133
	v_cvt_pk_bf16_f32 v133, v134, v135
	v_cvt_pk_bf16_f32 v134, v136, v137
	v_cvt_pk_bf16_f32 v135, v138, v139
	v_cvt_pk_bf16_f32 v168, v168, v169
	v_cvt_pk_bf16_f32 v169, v170, v171
	v_cvt_pk_bf16_f32 v170, v172, v173
	v_cvt_pk_bf16_f32 v171, v174, v175
	v_cvt_pk_bf16_f32 v140, v140, v141
	v_cvt_pk_bf16_f32 v141, v142, v143
	v_mov_b32_e32 v142, 0
	v_mov_b32_e32 v143, 0
	v_cvt_pk_bf16_f32 v176, v176, v177
	v_cvt_pk_bf16_f32 v177, v178, v179
	v_cvt_pk_bf16_f32 v178, v180, v181
	v_cvt_pk_bf16_f32 v179, v182, v183
	ds_bpermute_b32 v233, v15, v232
	ds_bpermute_b32 v227, v15, v226
	s_waitcnt lgkmcnt(2)
	v_mfma_f32_16x16x32_bf16 v[184:187], v[20:23], v[108:111], 0
	v_mfma_f32_16x16x32_bf16 v[188:191], v[24:27], v[108:111], 0
	v_mfma_f32_16x16x32_bf16 v[192:195], v[28:31], v[108:111], 0
	v_mfma_f32_16x16x32_bf16 v[196:199], v[32:35], v[108:111], 0
	v_mfma_f32_16x16x32_bf16 v[200:203], v[20:23], v[144:147], 0
	v_mfma_f32_16x16x32_bf16 v[204:207], v[24:27], v[144:147], 0
	v_mfma_f32_16x16x32_bf16 v[208:211], v[28:31], v[144:147], 0
	v_mfma_f32_16x16x32_bf16 v[212:215], v[32:35], v[144:147], 0
	ds_read2_b64 v[20:23], v11 offset0:16 offset1:20
	ds_read2_b64 v[24:27], v12 offset0:16 offset1:20
	ds_read2_b64 v[28:31], v13 offset0:16 offset1:20
	ds_read2_b64 v[32:35], v14 offset0:16 offset1:20
	v_mfma_f32_16x16x32_bf16 v[184:187], v[36:39], v[116:119], v[184:187]
	v_mfma_f32_16x16x32_bf16 v[188:191], v[40:43], v[116:119], v[188:191]
	v_mfma_f32_16x16x32_bf16 v[192:195], v[44:47], v[116:119], v[192:195]
	v_mfma_f32_16x16x32_bf16 v[196:199], v[48:51], v[116:119], v[196:199]
	v_mfma_f32_16x16x32_bf16 v[200:203], v[36:39], v[152:155], v[200:203]
	v_mfma_f32_16x16x32_bf16 v[204:207], v[40:43], v[152:155], v[204:207]
	v_mfma_f32_16x16x32_bf16 v[208:211], v[44:47], v[152:155], v[208:211]
	v_mfma_f32_16x16x32_bf16 v[212:215], v[48:51], v[152:155], v[212:215]
	ds_read2_b64 v[36:39], v11 offset0:24 offset1:28
	ds_read2_b64 v[40:43], v12 offset0:24 offset1:28
	ds_read2_b64 v[44:47], v13 offset0:24 offset1:28
	ds_read2_b64 v[48:51], v14 offset0:24 offset1:28
	s_waitcnt lgkmcnt(8)
	v_add_f32_e32 v232, v232, v233
	v_add_f32_e32 v226, v226, v227
	s_nop 0
	ds_bpermute_b32 v233, v16, v232
	ds_bpermute_b32 v227, v16, v226
	s_waitcnt lgkmcnt(6)
	v_mfma_f32_16x16x32_bf16 v[184:187], v[20:23], v[124:127], v[184:187]
	v_mfma_f32_16x16x32_bf16 v[188:191], v[24:27], v[124:127], v[188:191]
	v_mfma_f32_16x16x32_bf16 v[192:195], v[28:31], v[124:127], v[192:195]
	v_mfma_f32_16x16x32_bf16 v[196:199], v[32:35], v[124:127], v[196:199]
	v_mfma_f32_16x16x32_bf16 v[200:203], v[20:23], v[160:163], v[200:203]
	v_mfma_f32_16x16x32_bf16 v[204:207], v[24:27], v[160:163], v[204:207]
	v_mfma_f32_16x16x32_bf16 v[208:211], v[28:31], v[160:163], v[208:211]
	v_mfma_f32_16x16x32_bf16 v[212:215], v[32:35], v[160:163], v[212:215]
	ds_read2_b64 v[20:23], v11 offset0:32 offset1:36
	ds_read2_b64 v[24:27], v12 offset0:32 offset1:36
	ds_read2_b64 v[28:31], v13 offset0:32 offset1:36
	ds_read2_b64 v[32:35], v14 offset0:32 offset1:36
	s_waitcnt lgkmcnt(6)
	v_mfma_f32_16x16x32_bf16 v[184:187], v[36:39], v[132:135], v[184:187]
	v_mfma_f32_16x16x32_bf16 v[188:191], v[40:43], v[132:135], v[188:191]
	v_mfma_f32_16x16x32_bf16 v[192:195], v[44:47], v[132:135], v[192:195]
	v_mfma_f32_16x16x32_bf16 v[196:199], v[48:51], v[132:135], v[196:199]
	v_mfma_f32_16x16x32_bf16 v[200:203], v[36:39], v[168:171], v[200:203]
	v_mfma_f32_16x16x32_bf16 v[204:207], v[40:43], v[168:171], v[204:207]
	v_mfma_f32_16x16x32_bf16 v[208:211], v[44:47], v[168:171], v[208:211]
	v_mfma_f32_16x16x32_bf16 v[212:215], v[48:51], v[168:171], v[212:215]
	s_waitcnt lgkmcnt(0)
	v_mfma_f32_16x16x32_bf16 v[184:187], v[20:23], v[140:143], v[184:187]
	v_mfma_f32_16x16x32_bf16 v[188:191], v[24:27], v[140:143], v[188:191]
	v_mfma_f32_16x16x32_bf16 v[192:195], v[28:31], v[140:143], v[192:195]
	v_mfma_f32_16x16x32_bf16 v[196:199], v[32:35], v[140:143], v[196:199]
	v_mfma_f32_16x16x32_bf16 v[200:203], v[20:23], v[176:179], v[200:203]
	v_mfma_f32_16x16x32_bf16 v[204:207], v[24:27], v[176:179], v[204:207]
	v_mfma_f32_16x16x32_bf16 v[208:211], v[28:31], v[176:179], v[208:211]
	v_mfma_f32_16x16x32_bf16 v[212:215], v[32:35], v[176:179], v[212:215]
	v_add_f32_e32 v232, v232, v233
	v_add_f32_e32 v226, v226, v227
	v_add_f32_e32 v232, v232, v88
	v_add_f32_e32 v226, v226, v88
	v_rcp_f32_e32 v236, v232
	v_rcp_f32_e32 v230, v226
	v_mov_b32_e32 v237, v236
	v_mov_b32_e32 v231, v230
	s_nop 1
	v_pk_mul_f32 v[184:185], v[184:185], v[236:237]
	v_pk_mul_f32 v[186:187], v[186:187], v[236:237]
	v_pk_mul_f32 v[188:189], v[188:189], v[236:237]
	v_pk_mul_f32 v[190:191], v[190:191], v[236:237]
	v_pk_mul_f32 v[192:193], v[192:193], v[236:237]
	v_pk_mul_f32 v[194:195], v[194:195], v[236:237]
	v_pk_mul_f32 v[196:197], v[196:197], v[236:237]
	v_pk_mul_f32 v[198:199], v[198:199], v[236:237]
	v_pk_mul_f32 v[200:201], v[200:201], v[230:231]
	v_pk_mul_f32 v[202:203], v[202:203], v[230:231]
	v_pk_mul_f32 v[204:205], v[204:205], v[230:231]
	v_pk_mul_f32 v[206:207], v[206:207], v[230:231]
	v_pk_mul_f32 v[208:209], v[208:209], v[230:231]
	v_pk_mul_f32 v[210:211], v[210:211], v[230:231]
	v_pk_mul_f32 v[212:213], v[212:213], v[230:231]
	v_pk_mul_f32 v[214:215], v[214:215], v[230:231]
	v_cvt_pk_bf16_f32 v184, v184, v185
	v_cvt_pk_bf16_f32 v185, v186, v187
	v_cvt_pk_bf16_f32 v186, v188, v189
	v_cvt_pk_bf16_f32 v187, v190, v191
	v_cvt_pk_bf16_f32 v192, v192, v193
	v_cvt_pk_bf16_f32 v193, v194, v195
	v_cvt_pk_bf16_f32 v194, v196, v197
	v_cvt_pk_bf16_f32 v195, v198, v199
	v_cvt_pk_bf16_f32 v200, v200, v201
	v_cvt_pk_bf16_f32 v201, v202, v203
	v_cvt_pk_bf16_f32 v202, v204, v205
	v_cvt_pk_bf16_f32 v203, v206, v207
	v_cvt_pk_bf16_f32 v208, v208, v209
	v_cvt_pk_bf16_f32 v209, v210, v211
	v_cvt_pk_bf16_f32 v210, v212, v213
	v_cvt_pk_bf16_f32 v211, v214, v215
	s_nop 1
	v_permlane16_swap_b32 v184, v186
	v_permlane16_swap_b32 v185, v187
	v_permlane16_swap_b32 v192, v194
	v_permlane16_swap_b32 v193, v195
	v_permlane16_swap_b32 v200, v202
	v_permlane16_swap_b32 v201, v203
	v_permlane16_swap_b32 v208, v210
	v_permlane16_swap_b32 v209, v211
	global_store_dwordx4 v91, v[184:187], s[50:51]
	global_store_dwordx4 v91, v[192:195], s[50:51] offset:64
	global_store_dwordx4 v91, v[200:203], s[60:61]
	global_store_dwordx4 v91, v[208:211], s[60:61] offset:64
	s_add_u32 s50, s50, 0x20000
	s_addc_u32 s51, s51, 0
	s_add_u32 s60, s60, 0x20000
	s_addc_u32 s61, s61, 0
	ds_read_b128 v[20:23], v10 offset:4608
	ds_read_b128 v[24:27], v10 offset:4672
	ds_read_b128 v[28:31], v10 offset:6912
	ds_read_b128 v[32:35], v10 offset:6976
	ds_read_b128 v[36:39], v10 offset:9216
	ds_read_b128 v[40:43], v10 offset:9280
	ds_read_b128 v[44:47], v10 offset:11520
	ds_read_b128 v[48:51], v10 offset:11584
	ds_read_b128 v[216:219], v10 offset:13824
	ds_read_b128 v[220:223], v10 offset:13888
	s_waitcnt vmcnt(4)
	v_lshlrev_b32_e32 v234, 16, v92
	v_and_b32_e32 v235, 0xffff0000, v92
	v_pk_mul_f32 v[232:233], v[234:235], v[234:235]
	v_lshlrev_b32_e32 v228, 16, v100
	v_and_b32_e32 v229, 0xffff0000, v100
	v_pk_mul_f32 v[226:227], v[228:229], v[228:229]
	v_lshlrev_b32_e32 v234, 16, v93
	v_and_b32_e32 v235, 0xffff0000, v93
	v_pk_fma_f32 v[232:233], v[234:235], v[234:235], v[232:233]
	v_lshlrev_b32_e32 v228, 16, v101
	v_and_b32_e32 v229, 0xffff0000, v101
	v_pk_fma_f32 v[226:227], v[228:229], v[228:229], v[226:227]
	v_lshlrev_b32_e32 v234, 16, v94
	v_and_b32_e32 v235, 0xffff0000, v94
	v_pk_fma_f32 v[232:233], v[234:235], v[234:235], v[232:233]
	v_lshlrev_b32_e32 v228, 16, v102
	v_and_b32_e32 v229, 0xffff0000, v102
	v_pk_fma_f32 v[226:227], v[228:229], v[228:229], v[226:227]
	v_lshlrev_b32_e32 v234, 16, v95
	v_and_b32_e32 v235, 0xffff0000, v95
	v_pk_fma_f32 v[232:233], v[234:235], v[234:235], v[232:233]
	v_lshlrev_b32_e32 v228, 16, v103
	v_and_b32_e32 v229, 0xffff0000, v103
	v_pk_fma_f32 v[226:227], v[228:229], v[228:229], v[226:227]
	v_lshlrev_b32_e32 v234, 16, v96
	v_and_b32_e32 v235, 0xffff0000, v96
	v_pk_fma_f32 v[232:233], v[234:235], v[234:235], v[232:233]
	v_lshlrev_b32_e32 v228, 16, v104
	v_and_b32_e32 v229, 0xffff0000, v104
	v_pk_fma_f32 v[226:227], v[228:229], v[228:229], v[226:227]
	v_lshlrev_b32_e32 v234, 16, v97
	v_and_b32_e32 v235, 0xffff0000, v97
	v_pk_fma_f32 v[232:233], v[234:235], v[234:235], v[232:233]
	v_lshlrev_b32_e32 v228, 16, v105
	v_and_b32_e32 v229, 0xffff0000, v105
	v_pk_fma_f32 v[226:227], v[228:229], v[228:229], v[226:227]
	v_lshlrev_b32_e32 v234, 16, v98
	v_and_b32_e32 v235, 0xffff0000, v98
	v_pk_fma_f32 v[232:233], v[234:235], v[234:235], v[232:233]
	v_lshlrev_b32_e32 v228, 16, v106
	v_and_b32_e32 v229, 0xffff0000, v106
	v_pk_fma_f32 v[226:227], v[228:229], v[228:229], v[226:227]
	v_lshlrev_b32_e32 v234, 16, v99
	v_and_b32_e32 v235, 0xffff0000, v99
	v_pk_fma_f32 v[232:233], v[234:235], v[234:235], v[232:233]
	v_lshlrev_b32_e32 v228, 16, v107
	v_and_b32_e32 v229, 0xffff0000, v107
	v_pk_fma_f32 v[226:227], v[228:229], v[228:229], v[226:227]
	v_add_f32_e32 v232, v232, v233
	v_add_f32_e32 v226, v226, v227
	s_nop 0
	ds_bpermute_b32 v233, v15, v232
	ds_bpermute_b32 v227, v15, v226
	s_waitcnt lgkmcnt(6)
	v_mfma_f32_16x16x32_bf16 v[108:111], v[20:23], v[92:95], 0
	v_mfma_f32_16x16x32_bf16 v[112:115], v[28:31], v[92:95], 0
	v_mfma_f32_16x16x32_bf16 v[148:151], v[28:31], v[100:103], 0
	v_mfma_f32_16x16x32_bf16 v[116:119], v[36:39], v[92:95], 0
	v_mfma_f32_16x16x32_bf16 v[152:155], v[36:39], v[100:103], 0
	v_mfma_f32_16x16x32_bf16 v[108:111], v[24:27], v[96:99], v[108:111]
	v_mfma_f32_16x16x32_bf16 v[112:115], v[32:35], v[96:99], v[112:115]
	v_mfma_f32_16x16x32_bf16 v[148:151], v[32:35], v[104:107], v[148:151]
	v_mfma_f32_16x16x32_bf16 v[116:119], v[40:43], v[96:99], v[116:119]
	v_mfma_f32_16x16x32_bf16 v[152:155], v[40:43], v[104:107], v[152:155]
	ds_read_b128 v[20:23], v10 offset:16128
	ds_read_b128 v[24:27], v10 offset:16192
	ds_read_b128 v[28:31], v10 offset:18432
	ds_read_b128 v[32:35], v10 offset:18496
	ds_read_b128 v[36:39], v10 offset:20736
	ds_read_b128 v[40:43], v10 offset:20800
	s_waitcnt lgkmcnt(6)
	v_add_f32_e32 v232, v232, v233
	v_add_f32_e32 v226, v226, v227
	s_nop 0
	ds_bpermute_b32 v233, v16, v232
	ds_bpermute_b32 v227, v16, v226
	v_mfma_f32_16x16x32_bf16 v[120:123], v[44:47], v[92:95], 0
	v_mfma_f32_16x16x32_bf16 v[156:159], v[44:47], v[100:103], 0
	v_mfma_f32_16x16x32_bf16 v[124:127], v[216:219], v[92:95], 0
	v_mfma_f32_16x16x32_bf16 v[160:163], v[216:219], v[100:103], 0
	v_mfma_f32_16x16x32_bf16 v[120:123], v[48:51], v[96:99], v[120:123]
	v_mfma_f32_16x16x32_bf16 v[156:159], v[48:51], v[104:107], v[156:159]
	v_mfma_f32_16x16x32_bf16 v[124:127], v[220:223], v[96:99], v[124:127]
	v_mfma_f32_16x16x32_bf16 v[160:163], v[220:223], v[104:107], v[160:163]
	ds_read_b128 v[44:47], v10 offset:23040
	ds_read_b128 v[48:51], v10 offset:23104
	ds_read_b128 v[216:219], v10 offset:25344
	ds_read_b128 v[220:223], v10 offset:25408
	s_waitcnt lgkmcnt(6)
	v_mfma_f32_16x16x32_bf16 v[128:131], v[20:23], v[92:95], 0
	v_mfma_f32_16x16x32_bf16 v[164:167], v[20:23], v[100:103], 0
	v_mfma_f32_16x16x32_bf16 v[132:135], v[28:31], v[92:95], 0
	v_mfma_f32_16x16x32_bf16 v[168:171], v[28:31], v[100:103], 0
	v_mfma_f32_16x16x32_bf16 v[136:139], v[36:39], v[92:95], 0
	v_mfma_f32_16x16x32_bf16 v[172:175], v[36:39], v[100:103], 0
	v_mfma_f32_16x16x32_bf16 v[128:131], v[24:27], v[96:99], v[128:131]
	v_mfma_f32_16x16x32_bf16 v[164:167], v[24:27], v[104:107], v[164:167]
	v_mfma_f32_16x16x32_bf16 v[132:135], v[32:35], v[96:99], v[132:135]
	v_mfma_f32_16x16x32_bf16 v[168:171], v[32:35], v[104:107], v[168:171]
	v_mfma_f32_16x16x32_bf16 v[136:139], v[40:43], v[96:99], v[136:139]
	v_mfma_f32_16x16x32_bf16 v[172:175], v[40:43], v[104:107], v[172:175]
	s_waitcnt lgkmcnt(0)
	v_mfma_f32_16x16x32_bf16 v[140:143], v[44:47], v[92:95], 0
	v_mfma_f32_16x16x32_bf16 v[176:179], v[44:47], v[100:103], 0
	v_mfma_f32_16x16x32_bf16 v[180:183], v[216:219], v[100:103], 0
	v_mfma_f32_16x16x32_bf16 v[140:143], v[48:51], v[96:99], v[140:143]
	v_mfma_f32_16x16x32_bf16 v[176:179], v[48:51], v[104:107], v[176:179]
	v_mfma_f32_16x16x32_bf16 v[180:183], v[220:223], v[104:107], v[180:183]
	s_add_u32 s48, s48, 0x28000
	s_addc_u32 s49, s49, 0
	s_add_u32 s58, s58, 0x28000
	s_addc_u32 s59, s59, 0
	global_load_dwordx4 v[92:95], v8, s[48:49]
	global_load_dwordx4 v[96:99], v8, s[48:49] offset:64
	global_load_dwordx4 v[100:103], v8, s[58:59]
	global_load_dwordx4 v[104:107], v8, s[58:59] offset:64
	ds_read2_b64 v[20:23], v11 offset0:8 offset1:12
	ds_read2_b64 v[24:27], v12 offset0:8 offset1:12
	ds_read2_b64 v[28:31], v13 offset0:8 offset1:12
	ds_read2_b64 v[32:35], v14 offset0:8 offset1:12
	ds_read2_b64 v[36:39], v11 offset0:16 offset1:20
	ds_read2_b64 v[40:43], v12 offset0:16 offset1:20
	ds_read2_b64 v[44:47], v13 offset0:16 offset1:20
	ds_read2_b64 v[48:51], v14 offset0:16 offset1:20
	v_add_f32_e32 v232, v232, v233
	v_add_f32_e32 v226, v226, v227
	v_mul_f32_e32 v232, 0x3c800000, v232
	v_mul_f32_e32 v226, 0x3c800000, v226
	v_add_f32_e32 v232, 0x358637bd, v232
	v_add_f32_e32 v226, 0x358637bd, v226
	v_rsq_f32_e32 v236, v232
	v_rsq_f32_e32 v230, v226
	v_mov_b32_e32 v237, v236
	v_mov_b32_e32 v231, v230
	s_nop 1
	v_pk_fma_f32 v[108:109], v[108:109], v[236:237], v[52:53]
	v_pk_fma_f32 v[110:111], v[110:111], v[236:237], v[54:55]
	v_pk_fma_f32 v[148:149], v[148:149], v[230:231], v[52:53]
	v_pk_fma_f32 v[150:151], v[150:151], v[230:231], v[54:55]
	v_pk_fma_f32 v[112:113], v[112:113], v[236:237], v[56:57]
	v_pk_fma_f32 v[114:115], v[114:115], v[236:237], v[58:59]
	v_pk_fma_f32 v[152:153], v[152:153], v[230:231], v[56:57]
	v_pk_fma_f32 v[154:155], v[154:155], v[230:231], v[58:59]
	v_pk_fma_f32 v[116:117], v[116:117], v[236:237], v[60:61]
	v_pk_fma_f32 v[118:119], v[118:119], v[236:237], v[62:63]
	v_pk_fma_f32 v[156:157], v[156:157], v[230:231], v[60:61]
	v_pk_fma_f32 v[158:159], v[158:159], v[230:231], v[62:63]
	v_pk_fma_f32 v[120:121], v[120:121], v[236:237], v[64:65]
	v_pk_fma_f32 v[122:123], v[122:123], v[236:237], v[66:67]
	v_pk_fma_f32 v[160:161], v[160:161], v[230:231], v[64:65]
	v_pk_fma_f32 v[162:163], v[162:163], v[230:231], v[66:67]
	v_pk_fma_f32 v[124:125], v[124:125], v[236:237], v[68:69]
	v_pk_fma_f32 v[126:127], v[126:127], v[236:237], v[70:71]
	v_pk_fma_f32 v[164:165], v[164:165], v[230:231], v[68:69]
	v_pk_fma_f32 v[166:167], v[166:167], v[230:231], v[70:71]
	v_pk_fma_f32 v[128:129], v[128:129], v[236:237], v[72:73]
	v_pk_fma_f32 v[130:131], v[130:131], v[236:237], v[74:75]
	v_pk_fma_f32 v[168:169], v[168:169], v[230:231], v[72:73]
	v_pk_fma_f32 v[170:171], v[170:171], v[230:231], v[74:75]
	v_pk_fma_f32 v[132:133], v[132:133], v[236:237], v[76:77]
	v_pk_fma_f32 v[134:135], v[134:135], v[236:237], v[78:79]
	v_pk_fma_f32 v[172:173], v[172:173], v[230:231], v[76:77]
	v_pk_fma_f32 v[174:175], v[174:175], v[230:231], v[78:79]
	v_pk_fma_f32 v[136:137], v[136:137], v[236:237], v[80:81]
	v_pk_fma_f32 v[138:139], v[138:139], v[236:237], v[82:83]
	v_pk_fma_f32 v[176:177], v[176:177], v[230:231], v[80:81]
	v_pk_fma_f32 v[178:179], v[178:179], v[230:231], v[82:83]
	v_pk_fma_f32 v[140:141], v[140:141], v[236:237], v[84:85]
	v_pk_fma_f32 v[142:143], v[142:143], v[236:237], v[86:87]
	v_pk_fma_f32 v[180:181], v[180:181], v[230:231], v[84:85]
	v_pk_fma_f32 v[182:183], v[182:183], v[230:231], v[86:87]
	v_exp_f32_e32 v108, v108
	v_exp_f32_e32 v109, v109
	v_exp_f32_e32 v110, v110
	v_exp_f32_e32 v111, v111
	v_exp_f32_e32 v148, v148
	v_exp_f32_e32 v149, v149
	v_exp_f32_e32 v150, v150
	v_exp_f32_e32 v151, v151
	v_exp_f32_e32 v112, v112
	v_exp_f32_e32 v113, v113
	v_exp_f32_e32 v114, v114
	v_exp_f32_e32 v115, v115
	v_exp_f32_e32 v152, v152
	v_exp_f32_e32 v153, v153
	v_exp_f32_e32 v154, v154
	v_exp_f32_e32 v155, v155
	v_exp_f32_e32 v116, v116
	v_exp_f32_e32 v117, v117
	v_exp_f32_e32 v118, v118
	v_exp_f32_e32 v119, v119
	v_exp_f32_e32 v156, v156
	v_exp_f32_e32 v157, v157
	v_exp_f32_e32 v158, v158
	v_exp_f32_e32 v159, v159
	v_exp_f32_e32 v120, v120
	v_exp_f32_e32 v121, v121
	v_exp_f32_e32 v122, v122
	v_exp_f32_e32 v123, v123
	v_exp_f32_e32 v160, v160
	v_exp_f32_e32 v161, v161
	v_exp_f32_e32 v162, v162
	v_exp_f32_e32 v163, v163
	v_exp_f32_e32 v124, v124
	v_exp_f32_e32 v125, v125
	v_exp_f32_e32 v126, v126
	v_exp_f32_e32 v127, v127
	v_exp_f32_e32 v164, v164
	v_exp_f32_e32 v165, v165
	v_exp_f32_e32 v166, v166
	v_exp_f32_e32 v167, v167
	v_exp_f32_e32 v128, v128
	v_exp_f32_e32 v129, v129
	v_exp_f32_e32 v130, v130
	v_exp_f32_e32 v131, v131
	v_exp_f32_e32 v168, v168
	v_exp_f32_e32 v169, v169
	v_exp_f32_e32 v170, v170
	v_exp_f32_e32 v171, v171
	v_exp_f32_e32 v132, v132
	v_exp_f32_e32 v133, v133
	v_exp_f32_e32 v134, v134
	v_exp_f32_e32 v135, v135
	v_exp_f32_e32 v172, v172
	v_exp_f32_e32 v173, v173
	v_exp_f32_e32 v174, v174
	v_exp_f32_e32 v175, v175
	v_exp_f32_e32 v136, v136
	v_exp_f32_e32 v137, v137
	v_exp_f32_e32 v138, v138
	v_exp_f32_e32 v139, v139
	v_exp_f32_e32 v176, v176
	v_exp_f32_e32 v177, v177
	v_exp_f32_e32 v178, v178
	v_exp_f32_e32 v179, v179
	v_exp_f32_e32 v140, v140
	v_exp_f32_e32 v141, v141
	v_exp_f32_e32 v142, v142
	v_exp_f32_e32 v143, v143
	v_exp_f32_e32 v180, v180
	v_exp_f32_e32 v181, v181
	v_exp_f32_e32 v182, v182
	v_exp_f32_e32 v183, v183
	s_cmp_lg_u32 s36, 0
	s_cbranch_scc1 .Lat_m1
	v_mov_b32_e32 v108, 0
	v_mov_b32_e32 v109, 0
	v_mov_b32_e32 v110, 0
	v_mov_b32_e32 v111, 0
	v_mov_b32_e32 v112, 0
	v_mov_b32_e32 v113, 0
	v_mov_b32_e32 v114, 0
	v_mov_b32_e32 v115, 0
	v_mov_b32_e32 v116, 0
	v_mov_b32_e32 v117, 0
	v_mov_b32_e32 v118, 0
	v_mov_b32_e32 v119, 0
	v_mov_b32_e32 v120, 0
	v_mov_b32_e32 v121, 0
	v_mov_b32_e32 v122, 0
	v_mov_b32_e32 v123, 0
	v_mov_b32_e32 v124, 0
	v_mov_b32_e32 v125, 0
	v_mov_b32_e32 v126, 0
	v_mov_b32_e32 v127, 0
	v_mov_b32_e32 v128, 0
	v_mov_b32_e32 v129, 0
	v_mov_b32_e32 v130, 0
	v_mov_b32_e32 v131, 0
	v_mov_b32_e32 v148, 0
	v_mov_b32_e32 v149, 0
	v_mov_b32_e32 v150, 0
	v_mov_b32_e32 v151, 0
	v_mov_b32_e32 v152, 0
	v_mov_b32_e32 v153, 0
	v_mov_b32_e32 v154, 0
	v_mov_b32_e32 v155, 0
	v_mov_b32_e32 v156, 0
	v_mov_b32_e32 v157, 0
	v_mov_b32_e32 v158, 0
	v_mov_b32_e32 v159, 0
	v_mov_b32_e32 v160, 0
	v_mov_b32_e32 v161, 0
	v_mov_b32_e32 v162, 0
	v_mov_b32_e32 v163, 0
	v_mov_b32_e32 v164, 0
	v_mov_b32_e32 v165, 0
	v_mov_b32_e32 v166, 0
	v_mov_b32_e32 v167, 0
.Lat_m1:
	s_nop 0
	v_pk_add_f32 v[232:233], v[108:109], v[110:111]
	v_pk_add_f32 v[234:235], v[112:113], v[114:115]
	v_pk_add_f32 v[226:227], v[148:149], v[150:151]
	v_pk_add_f32 v[228:229], v[152:153], v[154:155]
	v_pk_add_f32 v[232:233], v[232:233], v[116:117]
	v_pk_add_f32 v[234:235], v[234:235], v[118:119]
	v_pk_add_f32 v[226:227], v[226:227], v[156:157]
	v_pk_add_f32 v[228:229], v[228:229], v[158:159]
	v_pk_add_f32 v[232:233], v[232:233], v[120:121]
	v_pk_add_f32 v[234:235], v[234:235], v[122:123]
	v_pk_add_f32 v[226:227], v[226:227], v[160:161]
	v_pk_add_f32 v[228:229], v[228:229], v[162:163]
	v_pk_add_f32 v[232:233], v[232:233], v[124:125]
	v_pk_add_f32 v[234:235], v[234:235], v[126:127]
	v_pk_add_f32 v[226:227], v[226:227], v[164:165]
	v_pk_add_f32 v[228:229], v[228:229], v[166:167]
	v_pk_add_f32 v[232:233], v[232:233], v[128:129]
	v_pk_add_f32 v[234:235], v[234:235], v[130:131]
	v_pk_add_f32 v[226:227], v[226:227], v[168:169]
	v_pk_add_f32 v[228:229], v[228:229], v[170:171]
	v_pk_add_f32 v[232:233], v[232:233], v[132:133]
	v_pk_add_f32 v[234:235], v[234:235], v[134:135]
	v_pk_add_f32 v[226:227], v[226:227], v[172:173]
	v_pk_add_f32 v[228:229], v[228:229], v[174:175]
	v_pk_add_f32 v[232:233], v[232:233], v[136:137]
	v_pk_add_f32 v[234:235], v[234:235], v[138:139]
	v_pk_add_f32 v[226:227], v[226:227], v[176:177]
	v_pk_add_f32 v[228:229], v[228:229], v[178:179]
	v_pk_add_f32 v[232:233], v[232:233], v[140:141]
	v_pk_add_f32 v[234:235], v[234:235], v[142:143]
	v_pk_add_f32 v[226:227], v[226:227], v[180:181]
	v_pk_add_f32 v[228:229], v[228:229], v[182:183]
	v_pk_add_f32 v[232:233], v[232:233], v[234:235]
	v_pk_add_f32 v[226:227], v[226:227], v[228:229]
	v_add_f32_e32 v232, v232, v233
	v_add_f32_e32 v226, v226, v227
	v_cvt_pk_bf16_f32 v108, v108, v109
	v_cvt_pk_bf16_f32 v109, v110, v111
	v_cvt_pk_bf16_f32 v110, v112, v113
	v_cvt_pk_bf16_f32 v111, v114, v115
	v_cvt_pk_bf16_f32 v146, v148, v149
	v_cvt_pk_bf16_f32 v147, v150, v151
	v_cvt_pk_bf16_f32 v116, v116, v117
	v_cvt_pk_bf16_f32 v117, v118, v119
	v_cvt_pk_bf16_f32 v118, v120, v121
	v_cvt_pk_bf16_f32 v119, v122, v123
	v_cvt_pk_bf16_f32 v152, v152, v153
	v_cvt_pk_bf16_f32 v153, v154, v155
	v_cvt_pk_bf16_f32 v154, v156, v157
	v_cvt_pk_bf16_f32 v155, v158, v159
	v_cvt_pk_bf16_f32 v124, v124, v125
	v_cvt_pk_bf16_f32 v125, v126, v127
	v_cvt_pk_bf16_f32 v126, v128, v129
	v_cvt_pk_bf16_f32 v127, v130, v131
	v_cvt_pk_bf16_f32 v160, v160, v161
	v_cvt_pk_bf16_f32 v161, v162, v163
	v_cvt_pk_bf16_f32 v162, v164, v165
	v_cvt_pk_bf16_f32 v163, v166, v167
	v_cvt_pk_bf16_f32 v132, v132, v133
	v_cvt_pk_bf16_f32 v133, v134, v135
	v_cvt_pk_bf16_f32 v134, v136, v137
	v_cvt_pk_bf16_f32 v135, v138, v139
	v_cvt_pk_bf16_f32 v168, v168, v169
	v_cvt_pk_bf16_f32 v169, v170, v171
	v_cvt_pk_bf16_f32 v170, v172, v173
	v_cvt_pk_bf16_f32 v171, v174, v175
	v_cvt_pk_bf16_f32 v140, v140, v141
	v_cvt_pk_bf16_f32 v141, v142, v143
	v_mov_b32_e32 v142, 0
	v_mov_b32_e32 v143, 0
	v_cvt_pk_bf16_f32 v176, v176, v177
	v_cvt_pk_bf16_f32 v177, v178, v179
	v_cvt_pk_bf16_f32 v178, v180, v181
	v_cvt_pk_bf16_f32 v179, v182, v183
	ds_bpermute_b32 v233, v15, v232
	ds_bpermute_b32 v227, v15, v226
	s_waitcnt lgkmcnt(2)
	v_mfma_f32_16x16x32_bf16 v[184:187], v[20:23], v[108:111], 0
	v_mfma_f32_16x16x32_bf16 v[188:191], v[24:27], v[108:111], 0
	v_mfma_f32_16x16x32_bf16 v[192:195], v[28:31], v[108:111], 0
	v_mfma_f32_16x16x32_bf16 v[196:199], v[32:35], v[108:111], 0
	v_mfma_f32_16x16x32_bf16 v[200:203], v[20:23], v[144:147], 0
	v_mfma_f32_16x16x32_bf16 v[204:207], v[24:27], v[144:147], 0
	v_mfma_f32_16x16x32_bf16 v[208:211], v[28:31], v[144:147], 0
	v_mfma_f32_16x16x32_bf16 v[212:215], v[32:35], v[144:147], 0
	ds_read2_b64 v[20:23], v11 offset0:24 offset1:28
	ds_read2_b64 v[24:27], v12 offset0:24 offset1:28
	ds_read2_b64 v[28:31], v13 offset0:24 offset1:28
	ds_read2_b64 v[32:35], v14 offset0:24 offset1:28
	v_mfma_f32_16x16x32_bf16 v[184:187], v[36:39], v[116:119], v[184:187]
	v_mfma_f32_16x16x32_bf16 v[188:191], v[40:43], v[116:119], v[188:191]
	v_mfma_f32_16x16x32_bf16 v[192:195], v[44:47], v[116:119], v[192:195]
	v_mfma_f32_16x16x32_bf16 v[196:199], v[48:51], v[116:119], v[196:199]
	v_mfma_f32_16x16x32_bf16 v[200:203], v[36:39], v[152:155], v[200:203]
	v_mfma_f32_16x16x32_bf16 v[204:207], v[40:43], v[152:155], v[204:207]
	v_mfma_f32_16x16x32_bf16 v[208:211], v[44:47], v[152:155], v[208:211]
	v_mfma_f32_16x16x32_bf16 v[212:215], v[48:51], v[152:155], v[212:215]
	ds_read2_b64 v[36:39], v11 offset0:32 offset1:36
	ds_read2_b64 v[40:43], v12 offset0:32 offset1:36
	ds_read2_b64 v[44:47], v13 offset0:32 offset1:36
	ds_read2_b64 v[48:51], v14 offset0:32 offset1:36
	s_waitcnt lgkmcnt(8)
	v_add_f32_e32 v232, v232, v233
	v_add_f32_e32 v226, v226, v227
	s_nop 0
	ds_bpermute_b32 v233, v16, v232
	ds_bpermute_b32 v227, v16, v226
	s_waitcnt lgkmcnt(6)
	v_mfma_f32_16x16x32_bf16 v[184:187], v[20:23], v[124:127], v[184:187]
	v_mfma_f32_16x16x32_bf16 v[188:191], v[24:27], v[124:127], v[188:191]
	v_mfma_f32_16x16x32_bf16 v[192:195], v[28:31], v[124:127], v[192:195]
	v_mfma_f32_16x16x32_bf16 v[196:199], v[32:35], v[124:127], v[196:199]
	v_mfma_f32_16x16x32_bf16 v[200:203], v[20:23], v[160:163], v[200:203]
	v_mfma_f32_16x16x32_bf16 v[204:207], v[24:27], v[160:163], v[204:207]
	v_mfma_f32_16x16x32_bf16 v[208:211], v[28:31], v[160:163], v[208:211]
	v_mfma_f32_16x16x32_bf16 v[212:215], v[32:35], v[160:163], v[212:215]
	ds_read2_b64 v[20:23], v11 offset0:40 offset1:44
	ds_read2_b64 v[24:27], v12 offset0:40 offset1:44
	ds_read2_b64 v[28:31], v13 offset0:40 offset1:44
	ds_read2_b64 v[32:35], v14 offset0:40 offset1:44
	s_waitcnt lgkmcnt(6)
	v_mfma_f32_16x16x32_bf16 v[184:187], v[36:39], v[132:135], v[184:187]
	v_mfma_f32_16x16x32_bf16 v[188:191], v[40:43], v[132:135], v[188:191]
	v_mfma_f32_16x16x32_bf16 v[192:195], v[44:47], v[132:135], v[192:195]
	v_mfma_f32_16x16x32_bf16 v[196:199], v[48:51], v[132:135], v[196:199]
	v_mfma_f32_16x16x32_bf16 v[200:203], v[36:39], v[168:171], v[200:203]
	v_mfma_f32_16x16x32_bf16 v[204:207], v[40:43], v[168:171], v[204:207]
	v_mfma_f32_16x16x32_bf16 v[208:211], v[44:47], v[168:171], v[208:211]
	v_mfma_f32_16x16x32_bf16 v[212:215], v[48:51], v[168:171], v[212:215]
	s_waitcnt lgkmcnt(0)
	v_mfma_f32_16x16x32_bf16 v[184:187], v[20:23], v[140:143], v[184:187]
	v_mfma_f32_16x16x32_bf16 v[188:191], v[24:27], v[140:143], v[188:191]
	v_mfma_f32_16x16x32_bf16 v[192:195], v[28:31], v[140:143], v[192:195]
	v_mfma_f32_16x16x32_bf16 v[196:199], v[32:35], v[140:143], v[196:199]
	v_mfma_f32_16x16x32_bf16 v[200:203], v[20:23], v[176:179], v[200:203]
	v_mfma_f32_16x16x32_bf16 v[204:207], v[24:27], v[176:179], v[204:207]
	v_mfma_f32_16x16x32_bf16 v[208:211], v[28:31], v[176:179], v[208:211]
	v_mfma_f32_16x16x32_bf16 v[212:215], v[32:35], v[176:179], v[212:215]
	v_add_f32_e32 v232, v232, v233
	v_add_f32_e32 v226, v226, v227
	v_add_f32_e32 v232, v232, v88
	v_add_f32_e32 v226, v226, v88
	v_rcp_f32_e32 v236, v232
	v_rcp_f32_e32 v230, v226
	v_mov_b32_e32 v237, v236
	v_mov_b32_e32 v231, v230
	s_nop 1
	v_pk_mul_f32 v[184:185], v[184:185], v[236:237]
	v_pk_mul_f32 v[186:187], v[186:187], v[236:237]
	v_pk_mul_f32 v[188:189], v[188:189], v[236:237]
	v_pk_mul_f32 v[190:191], v[190:191], v[236:237]
	v_pk_mul_f32 v[192:193], v[192:193], v[236:237]
	v_pk_mul_f32 v[194:195], v[194:195], v[236:237]
	v_pk_mul_f32 v[196:197], v[196:197], v[236:237]
	v_pk_mul_f32 v[198:199], v[198:199], v[236:237]
	v_pk_mul_f32 v[200:201], v[200:201], v[230:231]
	v_pk_mul_f32 v[202:203], v[202:203], v[230:231]
	v_pk_mul_f32 v[204:205], v[204:205], v[230:231]
	v_pk_mul_f32 v[206:207], v[206:207], v[230:231]
	v_pk_mul_f32 v[208:209], v[208:209], v[230:231]
	v_pk_mul_f32 v[210:211], v[210:211], v[230:231]
	v_pk_mul_f32 v[212:213], v[212:213], v[230:231]
	v_pk_mul_f32 v[214:215], v[214:215], v[230:231]
	v_cvt_pk_bf16_f32 v184, v184, v185
	v_cvt_pk_bf16_f32 v185, v186, v187
	v_cvt_pk_bf16_f32 v186, v188, v189
	v_cvt_pk_bf16_f32 v187, v190, v191
	v_cvt_pk_bf16_f32 v192, v192, v193
	v_cvt_pk_bf16_f32 v193, v194, v195
	v_cvt_pk_bf16_f32 v194, v196, v197
	v_cvt_pk_bf16_f32 v195, v198, v199
	v_cvt_pk_bf16_f32 v200, v200, v201
	v_cvt_pk_bf16_f32 v201, v202, v203
	v_cvt_pk_bf16_f32 v202, v204, v205
	v_cvt_pk_bf16_f32 v203, v206, v207
	v_cvt_pk_bf16_f32 v208, v208, v209
	v_cvt_pk_bf16_f32 v209, v210, v211
	v_cvt_pk_bf16_f32 v210, v212, v213
	v_cvt_pk_bf16_f32 v211, v214, v215
	s_nop 1
	v_permlane16_swap_b32 v184, v186
	v_permlane16_swap_b32 v185, v187
	v_permlane16_swap_b32 v192, v194
	v_permlane16_swap_b32 v193, v195
	v_permlane16_swap_b32 v200, v202
	v_permlane16_swap_b32 v201, v203
	v_permlane16_swap_b32 v208, v210
	v_permlane16_swap_b32 v209, v211
	global_store_dwordx4 v91, v[184:187], s[50:51]
	global_store_dwordx4 v91, v[192:195], s[50:51] offset:64
	global_store_dwordx4 v91, v[200:203], s[60:61]
	global_store_dwordx4 v91, v[208:211], s[60:61] offset:64
	s_add_u32 s50, s50, 0x20000
	s_addc_u32 s51, s51, 0
	s_add_u32 s60, s60, 0x20000
	s_addc_u32 s61, s61, 0
	ds_read_b128 v[20:23], v10 offset:9216
	ds_read_b128 v[24:27], v10 offset:9280
	ds_read_b128 v[28:31], v10 offset:11520
	ds_read_b128 v[32:35], v10 offset:11584
	ds_read_b128 v[36:39], v10 offset:13824
	ds_read_b128 v[40:43], v10 offset:13888
	ds_read_b128 v[44:47], v10 offset:16128
	ds_read_b128 v[48:51], v10 offset:16192
	ds_read_b128 v[216:219], v10 offset:18432
	ds_read_b128 v[220:223], v10 offset:18496
	s_waitcnt vmcnt(4)
	v_lshlrev_b32_e32 v234, 16, v92
	v_and_b32_e32 v235, 0xffff0000, v92
	v_pk_mul_f32 v[232:233], v[234:235], v[234:235]
	v_lshlrev_b32_e32 v228, 16, v100
	v_and_b32_e32 v229, 0xffff0000, v100
	v_pk_mul_f32 v[226:227], v[228:229], v[228:229]
	v_lshlrev_b32_e32 v234, 16, v93
	v_and_b32_e32 v235, 0xffff0000, v93
	v_pk_fma_f32 v[232:233], v[234:235], v[234:235], v[232:233]
	v_lshlrev_b32_e32 v228, 16, v101
	v_and_b32_e32 v229, 0xffff0000, v101
	v_pk_fma_f32 v[226:227], v[228:229], v[228:229], v[226:227]
	v_lshlrev_b32_e32 v234, 16, v94
	v_and_b32_e32 v235, 0xffff0000, v94
	v_pk_fma_f32 v[232:233], v[234:235], v[234:235], v[232:233]
	v_lshlrev_b32_e32 v228, 16, v102
	v_and_b32_e32 v229, 0xffff0000, v102
	v_pk_fma_f32 v[226:227], v[228:229], v[228:229], v[226:227]
	v_lshlrev_b32_e32 v234, 16, v95
	v_and_b32_e32 v235, 0xffff0000, v95
	v_pk_fma_f32 v[232:233], v[234:235], v[234:235], v[232:233]
	v_lshlrev_b32_e32 v228, 16, v103
	v_and_b32_e32 v229, 0xffff0000, v103
	v_pk_fma_f32 v[226:227], v[228:229], v[228:229], v[226:227]
	v_lshlrev_b32_e32 v234, 16, v96
	v_and_b32_e32 v235, 0xffff0000, v96
	v_pk_fma_f32 v[232:233], v[234:235], v[234:235], v[232:233]
	v_lshlrev_b32_e32 v228, 16, v104
	v_and_b32_e32 v229, 0xffff0000, v104
	v_pk_fma_f32 v[226:227], v[228:229], v[228:229], v[226:227]
	v_lshlrev_b32_e32 v234, 16, v97
	v_and_b32_e32 v235, 0xffff0000, v97
	v_pk_fma_f32 v[232:233], v[234:235], v[234:235], v[232:233]
	v_lshlrev_b32_e32 v228, 16, v105
	v_and_b32_e32 v229, 0xffff0000, v105
	v_pk_fma_f32 v[226:227], v[228:229], v[228:229], v[226:227]
	v_lshlrev_b32_e32 v234, 16, v98
	v_and_b32_e32 v235, 0xffff0000, v98
	v_pk_fma_f32 v[232:233], v[234:235], v[234:235], v[232:233]
	v_lshlrev_b32_e32 v228, 16, v106
	v_and_b32_e32 v229, 0xffff0000, v106
	v_pk_fma_f32 v[226:227], v[228:229], v[228:229], v[226:227]
	v_lshlrev_b32_e32 v234, 16, v99
	v_and_b32_e32 v235, 0xffff0000, v99
	v_pk_fma_f32 v[232:233], v[234:235], v[234:235], v[232:233]
	v_lshlrev_b32_e32 v228, 16, v107
	v_and_b32_e32 v229, 0xffff0000, v107
	v_pk_fma_f32 v[226:227], v[228:229], v[228:229], v[226:227]
	v_add_f32_e32 v232, v232, v233
	v_add_f32_e32 v226, v226, v227
	s_nop 0
	ds_bpermute_b32 v233, v15, v232
	ds_bpermute_b32 v227, v15, v226
	s_waitcnt lgkmcnt(6)
	v_mfma_f32_16x16x32_bf16 v[108:111], v[20:23], v[92:95], 0
	v_mfma_f32_16x16x32_bf16 v[112:115], v[28:31], v[92:95], 0
	v_mfma_f32_16x16x32_bf16 v[148:151], v[28:31], v[100:103], 0
	v_mfma_f32_16x16x32_bf16 v[116:119], v[36:39], v[92:95], 0
	v_mfma_f32_16x16x32_bf16 v[152:155], v[36:39], v[100:103], 0
	v_mfma_f32_16x16x32_bf16 v[108:111], v[24:27], v[96:99], v[108:111]
	v_mfma_f32_16x16x32_bf16 v[112:115], v[32:35], v[96:99], v[112:115]
	v_mfma_f32_16x16x32_bf16 v[148:151], v[32:35], v[104:107], v[148:151]
	v_mfma_f32_16x16x32_bf16 v[116:119], v[40:43], v[96:99], v[116:119]
	v_mfma_f32_16x16x32_bf16 v[152:155], v[40:43], v[104:107], v[152:155]
	ds_read_b128 v[20:23], v10 offset:20736
	ds_read_b128 v[24:27], v10 offset:20800
	ds_read_b128 v[28:31], v10 offset:23040
	ds_read_b128 v[32:35], v10 offset:23104
	ds_read_b128 v[36:39], v10 offset:25344
	ds_read_b128 v[40:43], v10 offset:25408
	s_waitcnt lgkmcnt(6)
	v_add_f32_e32 v232, v232, v233
	v_add_f32_e32 v226, v226, v227
	s_nop 0
	ds_bpermute_b32 v233, v16, v232
	ds_bpermute_b32 v227, v16, v226
	v_mfma_f32_16x16x32_bf16 v[120:123], v[44:47], v[92:95], 0
	v_mfma_f32_16x16x32_bf16 v[156:159], v[44:47], v[100:103], 0
	v_mfma_f32_16x16x32_bf16 v[124:127], v[216:219], v[92:95], 0
	v_mfma_f32_16x16x32_bf16 v[160:163], v[216:219], v[100:103], 0
	v_mfma_f32_16x16x32_bf16 v[120:123], v[48:51], v[96:99], v[120:123]
	v_mfma_f32_16x16x32_bf16 v[156:159], v[48:51], v[104:107], v[156:159]
	v_mfma_f32_16x16x32_bf16 v[124:127], v[220:223], v[96:99], v[124:127]
	v_mfma_f32_16x16x32_bf16 v[160:163], v[220:223], v[104:107], v[160:163]
	ds_read_b128 v[44:47], v10 offset:27648
	ds_read_b128 v[48:51], v10 offset:27712
	ds_read_b128 v[216:219], v10 offset:29952
	ds_read_b128 v[220:223], v10 offset:30016
	s_waitcnt lgkmcnt(6)
	v_mfma_f32_16x16x32_bf16 v[128:131], v[20:23], v[92:95], 0
	v_mfma_f32_16x16x32_bf16 v[164:167], v[20:23], v[100:103], 0
	v_mfma_f32_16x16x32_bf16 v[132:135], v[28:31], v[92:95], 0
	v_mfma_f32_16x16x32_bf16 v[168:171], v[28:31], v[100:103], 0
	v_mfma_f32_16x16x32_bf16 v[136:139], v[36:39], v[92:95], 0
	v_mfma_f32_16x16x32_bf16 v[172:175], v[36:39], v[100:103], 0
	v_mfma_f32_16x16x32_bf16 v[128:131], v[24:27], v[96:99], v[128:131]
	v_mfma_f32_16x16x32_bf16 v[164:167], v[24:27], v[104:107], v[164:167]
	v_mfma_f32_16x16x32_bf16 v[132:135], v[32:35], v[96:99], v[132:135]
	v_mfma_f32_16x16x32_bf16 v[168:171], v[32:35], v[104:107], v[168:171]
	v_mfma_f32_16x16x32_bf16 v[136:139], v[40:43], v[96:99], v[136:139]
	v_mfma_f32_16x16x32_bf16 v[172:175], v[40:43], v[104:107], v[172:175]
	s_waitcnt lgkmcnt(0)
	v_mfma_f32_16x16x32_bf16 v[140:143], v[44:47], v[92:95], 0
	v_mfma_f32_16x16x32_bf16 v[176:179], v[44:47], v[100:103], 0
	v_mfma_f32_16x16x32_bf16 v[180:183], v[216:219], v[100:103], 0
	v_mfma_f32_16x16x32_bf16 v[140:143], v[48:51], v[96:99], v[140:143]
	v_mfma_f32_16x16x32_bf16 v[176:179], v[48:51], v[104:107], v[176:179]
	v_mfma_f32_16x16x32_bf16 v[180:183], v[220:223], v[104:107], v[180:183]
	s_add_u32 s48, s48, 0x28000
	s_addc_u32 s49, s49, 0
	s_add_u32 s58, s58, 0x28000
	s_addc_u32 s59, s59, 0
	global_load_dwordx4 v[92:95], v8, s[48:49]
	global_load_dwordx4 v[96:99], v8, s[48:49] offset:64
	global_load_dwordx4 v[100:103], v8, s[58:59]
	global_load_dwordx4 v[104:107], v8, s[58:59] offset:64
	ds_read2_b64 v[20:23], v11 offset0:16 offset1:20
	ds_read2_b64 v[24:27], v12 offset0:16 offset1:20
	ds_read2_b64 v[28:31], v13 offset0:16 offset1:20
	ds_read2_b64 v[32:35], v14 offset0:16 offset1:20
	ds_read2_b64 v[36:39], v11 offset0:24 offset1:28
	ds_read2_b64 v[40:43], v12 offset0:24 offset1:28
	ds_read2_b64 v[44:47], v13 offset0:24 offset1:28
	ds_read2_b64 v[48:51], v14 offset0:24 offset1:28
	v_add_f32_e32 v232, v232, v233
	v_add_f32_e32 v226, v226, v227
	v_mul_f32_e32 v232, 0x3c800000, v232
	v_mul_f32_e32 v226, 0x3c800000, v226
	v_add_f32_e32 v232, 0x358637bd, v232
	v_add_f32_e32 v226, 0x358637bd, v226
	v_rsq_f32_e32 v236, v232
	v_rsq_f32_e32 v230, v226
	v_mov_b32_e32 v237, v236
	v_mov_b32_e32 v231, v230
	s_nop 1
	v_pk_fma_f32 v[108:109], v[108:109], v[236:237], v[52:53]
	v_pk_fma_f32 v[110:111], v[110:111], v[236:237], v[54:55]
	v_pk_fma_f32 v[148:149], v[148:149], v[230:231], v[52:53]
	v_pk_fma_f32 v[150:151], v[150:151], v[230:231], v[54:55]
	v_pk_fma_f32 v[112:113], v[112:113], v[236:237], v[56:57]
	v_pk_fma_f32 v[114:115], v[114:115], v[236:237], v[58:59]
	v_pk_fma_f32 v[152:153], v[152:153], v[230:231], v[56:57]
	v_pk_fma_f32 v[154:155], v[154:155], v[230:231], v[58:59]
	v_pk_fma_f32 v[116:117], v[116:117], v[236:237], v[60:61]
	v_pk_fma_f32 v[118:119], v[118:119], v[236:237], v[62:63]
	v_pk_fma_f32 v[156:157], v[156:157], v[230:231], v[60:61]
	v_pk_fma_f32 v[158:159], v[158:159], v[230:231], v[62:63]
	v_pk_fma_f32 v[120:121], v[120:121], v[236:237], v[64:65]
	v_pk_fma_f32 v[122:123], v[122:123], v[236:237], v[66:67]
	v_pk_fma_f32 v[160:161], v[160:161], v[230:231], v[64:65]
	v_pk_fma_f32 v[162:163], v[162:163], v[230:231], v[66:67]
	v_pk_fma_f32 v[124:125], v[124:125], v[236:237], v[68:69]
	v_pk_fma_f32 v[126:127], v[126:127], v[236:237], v[70:71]
	v_pk_fma_f32 v[164:165], v[164:165], v[230:231], v[68:69]
	v_pk_fma_f32 v[166:167], v[166:167], v[230:231], v[70:71]
	v_pk_fma_f32 v[128:129], v[128:129], v[236:237], v[72:73]
	v_pk_fma_f32 v[130:131], v[130:131], v[236:237], v[74:75]
	v_pk_fma_f32 v[168:169], v[168:169], v[230:231], v[72:73]
	v_pk_fma_f32 v[170:171], v[170:171], v[230:231], v[74:75]
	v_pk_fma_f32 v[132:133], v[132:133], v[236:237], v[76:77]
	v_pk_fma_f32 v[134:135], v[134:135], v[236:237], v[78:79]
	v_pk_fma_f32 v[172:173], v[172:173], v[230:231], v[76:77]
	v_pk_fma_f32 v[174:175], v[174:175], v[230:231], v[78:79]
	v_pk_fma_f32 v[136:137], v[136:137], v[236:237], v[80:81]
	v_pk_fma_f32 v[138:139], v[138:139], v[236:237], v[82:83]
	v_pk_fma_f32 v[176:177], v[176:177], v[230:231], v[80:81]
	v_pk_fma_f32 v[178:179], v[178:179], v[230:231], v[82:83]
	v_pk_fma_f32 v[140:141], v[140:141], v[236:237], v[84:85]
	v_pk_fma_f32 v[142:143], v[142:143], v[236:237], v[86:87]
	v_pk_fma_f32 v[180:181], v[180:181], v[230:231], v[84:85]
	v_pk_fma_f32 v[182:183], v[182:183], v[230:231], v[86:87]
	v_exp_f32_e32 v108, v108
	v_exp_f32_e32 v109, v109
	v_exp_f32_e32 v110, v110
	v_exp_f32_e32 v111, v111
	v_exp_f32_e32 v148, v148
	v_exp_f32_e32 v149, v149
	v_exp_f32_e32 v150, v150
	v_exp_f32_e32 v151, v151
	v_exp_f32_e32 v112, v112
	v_exp_f32_e32 v113, v113
	v_exp_f32_e32 v114, v114
	v_exp_f32_e32 v115, v115
	v_exp_f32_e32 v152, v152
	v_exp_f32_e32 v153, v153
	v_exp_f32_e32 v154, v154
	v_exp_f32_e32 v155, v155
	v_exp_f32_e32 v116, v116
	v_exp_f32_e32 v117, v117
	v_exp_f32_e32 v118, v118
	v_exp_f32_e32 v119, v119
	v_exp_f32_e32 v156, v156
	v_exp_f32_e32 v157, v157
	v_exp_f32_e32 v158, v158
	v_exp_f32_e32 v159, v159
	v_exp_f32_e32 v120, v120
	v_exp_f32_e32 v121, v121
	v_exp_f32_e32 v122, v122
	v_exp_f32_e32 v123, v123
	v_exp_f32_e32 v160, v160
	v_exp_f32_e32 v161, v161
	v_exp_f32_e32 v162, v162
	v_exp_f32_e32 v163, v163
	v_exp_f32_e32 v124, v124
	v_exp_f32_e32 v125, v125
	v_exp_f32_e32 v126, v126
	v_exp_f32_e32 v127, v127
	v_exp_f32_e32 v164, v164
	v_exp_f32_e32 v165, v165
	v_exp_f32_e32 v166, v166
	v_exp_f32_e32 v167, v167
	v_exp_f32_e32 v128, v128
	v_exp_f32_e32 v129, v129
	v_exp_f32_e32 v130, v130
	v_exp_f32_e32 v131, v131
	v_exp_f32_e32 v168, v168
	v_exp_f32_e32 v169, v169
	v_exp_f32_e32 v170, v170
	v_exp_f32_e32 v171, v171
	v_exp_f32_e32 v132, v132
	v_exp_f32_e32 v133, v133
	v_exp_f32_e32 v134, v134
	v_exp_f32_e32 v135, v135
	v_exp_f32_e32 v172, v172
	v_exp_f32_e32 v173, v173
	v_exp_f32_e32 v174, v174
	v_exp_f32_e32 v175, v175
	v_exp_f32_e32 v136, v136
	v_exp_f32_e32 v137, v137
	v_exp_f32_e32 v138, v138
	v_exp_f32_e32 v139, v139
	v_exp_f32_e32 v176, v176
	v_exp_f32_e32 v177, v177
	v_exp_f32_e32 v178, v178
	v_exp_f32_e32 v179, v179
	v_exp_f32_e32 v140, v140
	v_exp_f32_e32 v141, v141
	v_exp_f32_e32 v142, v142
	v_exp_f32_e32 v143, v143
	v_exp_f32_e32 v180, v180
	v_exp_f32_e32 v181, v181
	v_exp_f32_e32 v182, v182
	v_exp_f32_e32 v183, v183
	s_cmp_lg_u32 s36, 0
	s_cbranch_scc1 .Lat_m2
	v_mov_b32_e32 v108, 0
	v_mov_b32_e32 v109, 0
	v_mov_b32_e32 v110, 0
	v_mov_b32_e32 v111, 0
	v_mov_b32_e32 v112, 0
	v_mov_b32_e32 v113, 0
	v_mov_b32_e32 v114, 0
	v_mov_b32_e32 v115, 0
	v_mov_b32_e32 v116, 0
	v_mov_b32_e32 v117, 0
	v_mov_b32_e32 v118, 0
	v_mov_b32_e32 v119, 0
	v_mov_b32_e32 v120, 0
	v_mov_b32_e32 v121, 0
	v_mov_b32_e32 v122, 0
	v_mov_b32_e32 v123, 0
	v_mov_b32_e32 v148, 0
	v_mov_b32_e32 v149, 0
	v_mov_b32_e32 v150, 0
	v_mov_b32_e32 v151, 0
	v_mov_b32_e32 v152, 0
	v_mov_b32_e32 v153, 0
	v_mov_b32_e32 v154, 0
	v_mov_b32_e32 v155, 0
	v_mov_b32_e32 v156, 0
	v_mov_b32_e32 v157, 0
	v_mov_b32_e32 v158, 0
	v_mov_b32_e32 v159, 0
.Lat_m2:
	s_nop 0
	v_pk_add_f32 v[232:233], v[108:109], v[110:111]
	v_pk_add_f32 v[234:235], v[112:113], v[114:115]
	v_pk_add_f32 v[226:227], v[148:149], v[150:151]
	v_pk_add_f32 v[228:229], v[152:153], v[154:155]
	v_pk_add_f32 v[232:233], v[232:233], v[116:117]
	v_pk_add_f32 v[234:235], v[234:235], v[118:119]
	v_pk_add_f32 v[226:227], v[226:227], v[156:157]
	v_pk_add_f32 v[228:229], v[228:229], v[158:159]
	v_pk_add_f32 v[232:233], v[232:233], v[120:121]
	v_pk_add_f32 v[234:235], v[234:235], v[122:123]
	v_pk_add_f32 v[226:227], v[226:227], v[160:161]
	v_pk_add_f32 v[228:229], v[228:229], v[162:163]
	v_pk_add_f32 v[232:233], v[232:233], v[124:125]
	v_pk_add_f32 v[234:235], v[234:235], v[126:127]
	v_pk_add_f32 v[226:227], v[226:227], v[164:165]
	v_pk_add_f32 v[228:229], v[228:229], v[166:167]
	v_pk_add_f32 v[232:233], v[232:233], v[128:129]
	v_pk_add_f32 v[234:235], v[234:235], v[130:131]
	v_pk_add_f32 v[226:227], v[226:227], v[168:169]
	v_pk_add_f32 v[228:229], v[228:229], v[170:171]
	v_pk_add_f32 v[232:233], v[232:233], v[132:133]
	v_pk_add_f32 v[234:235], v[234:235], v[134:135]
	v_pk_add_f32 v[226:227], v[226:227], v[172:173]
	v_pk_add_f32 v[228:229], v[228:229], v[174:175]
	v_pk_add_f32 v[232:233], v[232:233], v[136:137]
	v_pk_add_f32 v[234:235], v[234:235], v[138:139]
	v_pk_add_f32 v[226:227], v[226:227], v[176:177]
	v_pk_add_f32 v[228:229], v[228:229], v[178:179]
	v_pk_add_f32 v[232:233], v[232:233], v[140:141]
	v_pk_add_f32 v[234:235], v[234:235], v[142:143]
	v_pk_add_f32 v[226:227], v[226:227], v[180:181]
	v_pk_add_f32 v[228:229], v[228:229], v[182:183]
	v_pk_add_f32 v[232:233], v[232:233], v[234:235]
	v_pk_add_f32 v[226:227], v[226:227], v[228:229]
	v_add_f32_e32 v232, v232, v233
	v_add_f32_e32 v226, v226, v227
	v_cvt_pk_bf16_f32 v108, v108, v109
	v_cvt_pk_bf16_f32 v109, v110, v111
	v_cvt_pk_bf16_f32 v110, v112, v113
	v_cvt_pk_bf16_f32 v111, v114, v115
	v_cvt_pk_bf16_f32 v146, v148, v149
	v_cvt_pk_bf16_f32 v147, v150, v151
	v_cvt_pk_bf16_f32 v116, v116, v117
	v_cvt_pk_bf16_f32 v117, v118, v119
	v_cvt_pk_bf16_f32 v118, v120, v121
	v_cvt_pk_bf16_f32 v119, v122, v123
	v_cvt_pk_bf16_f32 v152, v152, v153
	v_cvt_pk_bf16_f32 v153, v154, v155
	v_cvt_pk_bf16_f32 v154, v156, v157
	v_cvt_pk_bf16_f32 v155, v158, v159
	v_cvt_pk_bf16_f32 v124, v124, v125
	v_cvt_pk_bf16_f32 v125, v126, v127
	v_cvt_pk_bf16_f32 v126, v128, v129
	v_cvt_pk_bf16_f32 v127, v130, v131
	v_cvt_pk_bf16_f32 v160, v160, v161
	v_cvt_pk_bf16_f32 v161, v162, v163
	v_cvt_pk_bf16_f32 v162, v164, v165
	v_cvt_pk_bf16_f32 v163, v166, v167
	v_cvt_pk_bf16_f32 v132, v132, v133
	v_cvt_pk_bf16_f32 v133, v134, v135
	v_cvt_pk_bf16_f32 v134, v136, v137
	v_cvt_pk_bf16_f32 v135, v138, v139
	v_cvt_pk_bf16_f32 v168, v168, v169
	v_cvt_pk_bf16_f32 v169, v170, v171
	v_cvt_pk_bf16_f32 v170, v172, v173
	v_cvt_pk_bf16_f32 v171, v174, v175
	v_cvt_pk_bf16_f32 v140, v140, v141
	v_cvt_pk_bf16_f32 v141, v142, v143
	v_mov_b32_e32 v142, 0
	v_mov_b32_e32 v143, 0
	v_cvt_pk_bf16_f32 v176, v176, v177
	v_cvt_pk_bf16_f32 v177, v178, v179
	v_cvt_pk_bf16_f32 v178, v180, v181
	v_cvt_pk_bf16_f32 v179, v182, v183
	ds_bpermute_b32 v233, v15, v232
	ds_bpermute_b32 v227, v15, v226
	s_waitcnt lgkmcnt(2)
	v_mfma_f32_16x16x32_bf16 v[184:187], v[20:23], v[108:111], 0
	v_mfma_f32_16x16x32_bf16 v[188:191], v[24:27], v[108:111], 0
	v_mfma_f32_16x16x32_bf16 v[192:195], v[28:31], v[108:111], 0
	v_mfma_f32_16x16x32_bf16 v[196:199], v[32:35], v[108:111], 0
	v_mfma_f32_16x16x32_bf16 v[200:203], v[20:23], v[144:147], 0
	v_mfma_f32_16x16x32_bf16 v[204:207], v[24:27], v[144:147], 0
	v_mfma_f32_16x16x32_bf16 v[208:211], v[28:31], v[144:147], 0
	v_mfma_f32_16x16x32_bf16 v[212:215], v[32:35], v[144:147], 0
	ds_read2_b64 v[20:23], v11 offset0:32 offset1:36
	ds_read2_b64 v[24:27], v12 offset0:32 offset1:36
	ds_read2_b64 v[28:31], v13 offset0:32 offset1:36
	ds_read2_b64 v[32:35], v14 offset0:32 offset1:36
	v_mfma_f32_16x16x32_bf16 v[184:187], v[36:39], v[116:119], v[184:187]
	v_mfma_f32_16x16x32_bf16 v[188:191], v[40:43], v[116:119], v[188:191]
	v_mfma_f32_16x16x32_bf16 v[192:195], v[44:47], v[116:119], v[192:195]
	v_mfma_f32_16x16x32_bf16 v[196:199], v[48:51], v[116:119], v[196:199]
	v_mfma_f32_16x16x32_bf16 v[200:203], v[36:39], v[152:155], v[200:203]
	v_mfma_f32_16x16x32_bf16 v[204:207], v[40:43], v[152:155], v[204:207]
	v_mfma_f32_16x16x32_bf16 v[208:211], v[44:47], v[152:155], v[208:211]
	v_mfma_f32_16x16x32_bf16 v[212:215], v[48:51], v[152:155], v[212:215]
	ds_read2_b64 v[36:39], v11 offset0:40 offset1:44
	ds_read2_b64 v[40:43], v12 offset0:40 offset1:44
	ds_read2_b64 v[44:47], v13 offset0:40 offset1:44
	ds_read2_b64 v[48:51], v14 offset0:40 offset1:44
	s_waitcnt lgkmcnt(8)
	v_add_f32_e32 v232, v232, v233
	v_add_f32_e32 v226, v226, v227
	s_nop 0
	ds_bpermute_b32 v233, v16, v232
	ds_bpermute_b32 v227, v16, v226
	s_waitcnt lgkmcnt(6)
	v_mfma_f32_16x16x32_bf16 v[184:187], v[20:23], v[124:127], v[184:187]
	v_mfma_f32_16x16x32_bf16 v[188:191], v[24:27], v[124:127], v[188:191]
	v_mfma_f32_16x16x32_bf16 v[192:195], v[28:31], v[124:127], v[192:195]
	v_mfma_f32_16x16x32_bf16 v[196:199], v[32:35], v[124:127], v[196:199]
	v_mfma_f32_16x16x32_bf16 v[200:203], v[20:23], v[160:163], v[200:203]
	v_mfma_f32_16x16x32_bf16 v[204:207], v[24:27], v[160:163], v[204:207]
	v_mfma_f32_16x16x32_bf16 v[208:211], v[28:31], v[160:163], v[208:211]
	v_mfma_f32_16x16x32_bf16 v[212:215], v[32:35], v[160:163], v[212:215]
	ds_read2_b64 v[20:23], v11 offset0:48 offset1:52
	ds_read2_b64 v[24:27], v12 offset0:48 offset1:52
	ds_read2_b64 v[28:31], v13 offset0:48 offset1:52
	ds_read2_b64 v[32:35], v14 offset0:48 offset1:52
	s_waitcnt lgkmcnt(6)
	v_mfma_f32_16x16x32_bf16 v[184:187], v[36:39], v[132:135], v[184:187]
	v_mfma_f32_16x16x32_bf16 v[188:191], v[40:43], v[132:135], v[188:191]
	v_mfma_f32_16x16x32_bf16 v[192:195], v[44:47], v[132:135], v[192:195]
	v_mfma_f32_16x16x32_bf16 v[196:199], v[48:51], v[132:135], v[196:199]
	v_mfma_f32_16x16x32_bf16 v[200:203], v[36:39], v[168:171], v[200:203]
	v_mfma_f32_16x16x32_bf16 v[204:207], v[40:43], v[168:171], v[204:207]
	v_mfma_f32_16x16x32_bf16 v[208:211], v[44:47], v[168:171], v[208:211]
	v_mfma_f32_16x16x32_bf16 v[212:215], v[48:51], v[168:171], v[212:215]
	s_waitcnt lgkmcnt(0)
	v_mfma_f32_16x16x32_bf16 v[184:187], v[20:23], v[140:143], v[184:187]
	v_mfma_f32_16x16x32_bf16 v[188:191], v[24:27], v[140:143], v[188:191]
	v_mfma_f32_16x16x32_bf16 v[192:195], v[28:31], v[140:143], v[192:195]
	v_mfma_f32_16x16x32_bf16 v[196:199], v[32:35], v[140:143], v[196:199]
	v_mfma_f32_16x16x32_bf16 v[200:203], v[20:23], v[176:179], v[200:203]
	v_mfma_f32_16x16x32_bf16 v[204:207], v[24:27], v[176:179], v[204:207]
	v_mfma_f32_16x16x32_bf16 v[208:211], v[28:31], v[176:179], v[208:211]
	v_mfma_f32_16x16x32_bf16 v[212:215], v[32:35], v[176:179], v[212:215]
	v_add_f32_e32 v232, v232, v233
	v_add_f32_e32 v226, v226, v227
	v_add_f32_e32 v232, v232, v88
	v_add_f32_e32 v226, v226, v88
	v_rcp_f32_e32 v236, v232
	v_rcp_f32_e32 v230, v226
	v_mov_b32_e32 v237, v236
	v_mov_b32_e32 v231, v230
	s_nop 1
	v_pk_mul_f32 v[184:185], v[184:185], v[236:237]
	v_pk_mul_f32 v[186:187], v[186:187], v[236:237]
	v_pk_mul_f32 v[188:189], v[188:189], v[236:237]
	v_pk_mul_f32 v[190:191], v[190:191], v[236:237]
	v_pk_mul_f32 v[192:193], v[192:193], v[236:237]
	v_pk_mul_f32 v[194:195], v[194:195], v[236:237]
	v_pk_mul_f32 v[196:197], v[196:197], v[236:237]
	v_pk_mul_f32 v[198:199], v[198:199], v[236:237]
	v_pk_mul_f32 v[200:201], v[200:201], v[230:231]
	v_pk_mul_f32 v[202:203], v[202:203], v[230:231]
	v_pk_mul_f32 v[204:205], v[204:205], v[230:231]
	v_pk_mul_f32 v[206:207], v[206:207], v[230:231]
	v_pk_mul_f32 v[208:209], v[208:209], v[230:231]
	v_pk_mul_f32 v[210:211], v[210:211], v[230:231]
	v_pk_mul_f32 v[212:213], v[212:213], v[230:231]
	v_pk_mul_f32 v[214:215], v[214:215], v[230:231]
	v_cvt_pk_bf16_f32 v184, v184, v185
	v_cvt_pk_bf16_f32 v185, v186, v187
	v_cvt_pk_bf16_f32 v186, v188, v189
	v_cvt_pk_bf16_f32 v187, v190, v191
	v_cvt_pk_bf16_f32 v192, v192, v193
	v_cvt_pk_bf16_f32 v193, v194, v195
	v_cvt_pk_bf16_f32 v194, v196, v197
	v_cvt_pk_bf16_f32 v195, v198, v199
	v_cvt_pk_bf16_f32 v200, v200, v201
	v_cvt_pk_bf16_f32 v201, v202, v203
	v_cvt_pk_bf16_f32 v202, v204, v205
	v_cvt_pk_bf16_f32 v203, v206, v207
	v_cvt_pk_bf16_f32 v208, v208, v209
	v_cvt_pk_bf16_f32 v209, v210, v211
	v_cvt_pk_bf16_f32 v210, v212, v213
	v_cvt_pk_bf16_f32 v211, v214, v215
	s_nop 1
	v_permlane16_swap_b32 v184, v186
	v_permlane16_swap_b32 v185, v187
	v_permlane16_swap_b32 v192, v194
	v_permlane16_swap_b32 v193, v195
	v_permlane16_swap_b32 v200, v202
	v_permlane16_swap_b32 v201, v203
	v_permlane16_swap_b32 v208, v210
	v_permlane16_swap_b32 v209, v211
	global_store_dwordx4 v91, v[184:187], s[50:51]
	global_store_dwordx4 v91, v[192:195], s[50:51] offset:64
	global_store_dwordx4 v91, v[200:203], s[60:61]
	global_store_dwordx4 v91, v[208:211], s[60:61] offset:64
	s_add_u32 s50, s50, 0x20000
	s_addc_u32 s51, s51, 0
	s_add_u32 s60, s60, 0x20000
	s_addc_u32 s61, s61, 0
	ds_read_b128 v[20:23], v10 offset:13824
	ds_read_b128 v[24:27], v10 offset:13888
	ds_read_b128 v[28:31], v10 offset:16128
	ds_read_b128 v[32:35], v10 offset:16192
	ds_read_b128 v[36:39], v10 offset:18432
	ds_read_b128 v[40:43], v10 offset:18496
	ds_read_b128 v[44:47], v10 offset:20736
	ds_read_b128 v[48:51], v10 offset:20800
	ds_read_b128 v[216:219], v10 offset:23040
	ds_read_b128 v[220:223], v10 offset:23104
	s_waitcnt vmcnt(4)
	v_lshlrev_b32_e32 v234, 16, v92
	v_and_b32_e32 v235, 0xffff0000, v92
	v_pk_mul_f32 v[232:233], v[234:235], v[234:235]
	v_lshlrev_b32_e32 v228, 16, v100
	v_and_b32_e32 v229, 0xffff0000, v100
	v_pk_mul_f32 v[226:227], v[228:229], v[228:229]
	v_lshlrev_b32_e32 v234, 16, v93
	v_and_b32_e32 v235, 0xffff0000, v93
	v_pk_fma_f32 v[232:233], v[234:235], v[234:235], v[232:233]
	v_lshlrev_b32_e32 v228, 16, v101
	v_and_b32_e32 v229, 0xffff0000, v101
	v_pk_fma_f32 v[226:227], v[228:229], v[228:229], v[226:227]
	v_lshlrev_b32_e32 v234, 16, v94
	v_and_b32_e32 v235, 0xffff0000, v94
	v_pk_fma_f32 v[232:233], v[234:235], v[234:235], v[232:233]
	v_lshlrev_b32_e32 v228, 16, v102
	v_and_b32_e32 v229, 0xffff0000, v102
	v_pk_fma_f32 v[226:227], v[228:229], v[228:229], v[226:227]
	v_lshlrev_b32_e32 v234, 16, v95
	v_and_b32_e32 v235, 0xffff0000, v95
	v_pk_fma_f32 v[232:233], v[234:235], v[234:235], v[232:233]
	v_lshlrev_b32_e32 v228, 16, v103
	v_and_b32_e32 v229, 0xffff0000, v103
	v_pk_fma_f32 v[226:227], v[228:229], v[228:229], v[226:227]
	v_lshlrev_b32_e32 v234, 16, v96
	v_and_b32_e32 v235, 0xffff0000, v96
	v_pk_fma_f32 v[232:233], v[234:235], v[234:235], v[232:233]
	v_lshlrev_b32_e32 v228, 16, v104
	v_and_b32_e32 v229, 0xffff0000, v104
	v_pk_fma_f32 v[226:227], v[228:229], v[228:229], v[226:227]
	v_lshlrev_b32_e32 v234, 16, v97
	v_and_b32_e32 v235, 0xffff0000, v97
	v_pk_fma_f32 v[232:233], v[234:235], v[234:235], v[232:233]
	v_lshlrev_b32_e32 v228, 16, v105
	v_and_b32_e32 v229, 0xffff0000, v105
	v_pk_fma_f32 v[226:227], v[228:229], v[228:229], v[226:227]
	v_lshlrev_b32_e32 v234, 16, v98
	v_and_b32_e32 v235, 0xffff0000, v98
	v_pk_fma_f32 v[232:233], v[234:235], v[234:235], v[232:233]
	v_lshlrev_b32_e32 v228, 16, v106
	v_and_b32_e32 v229, 0xffff0000, v106
	v_pk_fma_f32 v[226:227], v[228:229], v[228:229], v[226:227]
	v_lshlrev_b32_e32 v234, 16, v99
	v_and_b32_e32 v235, 0xffff0000, v99
	v_pk_fma_f32 v[232:233], v[234:235], v[234:235], v[232:233]
	v_lshlrev_b32_e32 v228, 16, v107
	v_and_b32_e32 v229, 0xffff0000, v107
	v_pk_fma_f32 v[226:227], v[228:229], v[228:229], v[226:227]
	v_add_f32_e32 v232, v232, v233
	v_add_f32_e32 v226, v226, v227
	s_nop 0
	ds_bpermute_b32 v233, v15, v232
	ds_bpermute_b32 v227, v15, v226
	s_waitcnt lgkmcnt(6)
	v_mfma_f32_16x16x32_bf16 v[108:111], v[20:23], v[92:95], 0
	v_mfma_f32_16x16x32_bf16 v[112:115], v[28:31], v[92:95], 0
	v_mfma_f32_16x16x32_bf16 v[148:151], v[28:31], v[100:103], 0
	v_mfma_f32_16x16x32_bf16 v[116:119], v[36:39], v[92:95], 0
	v_mfma_f32_16x16x32_bf16 v[152:155], v[36:39], v[100:103], 0
	v_mfma_f32_16x16x32_bf16 v[108:111], v[24:27], v[96:99], v[108:111]
	v_mfma_f32_16x16x32_bf16 v[112:115], v[32:35], v[96:99], v[112:115]
	v_mfma_f32_16x16x32_bf16 v[148:151], v[32:35], v[104:107], v[148:151]
	v_mfma_f32_16x16x32_bf16 v[116:119], v[40:43], v[96:99], v[116:119]
	v_mfma_f32_16x16x32_bf16 v[152:155], v[40:43], v[104:107], v[152:155]
	ds_read_b128 v[20:23], v10 offset:25344
	ds_read_b128 v[24:27], v10 offset:25408
	ds_read_b128 v[28:31], v10 offset:27648
	ds_read_b128 v[32:35], v10 offset:27712
	ds_read_b128 v[36:39], v10 offset:29952
	ds_read_b128 v[40:43], v10 offset:30016
	s_waitcnt lgkmcnt(6)
	v_add_f32_e32 v232, v232, v233
	v_add_f32_e32 v226, v226, v227
	s_nop 0
	ds_bpermute_b32 v233, v16, v232
	ds_bpermute_b32 v227, v16, v226
	v_mfma_f32_16x16x32_bf16 v[120:123], v[44:47], v[92:95], 0
	v_mfma_f32_16x16x32_bf16 v[156:159], v[44:47], v[100:103], 0
	v_mfma_f32_16x16x32_bf16 v[124:127], v[216:219], v[92:95], 0
	v_mfma_f32_16x16x32_bf16 v[160:163], v[216:219], v[100:103], 0
	v_mfma_f32_16x16x32_bf16 v[120:123], v[48:51], v[96:99], v[120:123]
	v_mfma_f32_16x16x32_bf16 v[156:159], v[48:51], v[104:107], v[156:159]
	v_mfma_f32_16x16x32_bf16 v[124:127], v[220:223], v[96:99], v[124:127]
	v_mfma_f32_16x16x32_bf16 v[160:163], v[220:223], v[104:107], v[160:163]
	ds_read_b128 v[44:47], v10 offset:32256
	ds_read_b128 v[48:51], v10 offset:32320
	ds_read_b128 v[216:219], v10 offset:34560
	ds_read_b128 v[220:223], v10 offset:34624
	s_waitcnt lgkmcnt(6)
	v_mfma_f32_16x16x32_bf16 v[128:131], v[20:23], v[92:95], 0
	v_mfma_f32_16x16x32_bf16 v[164:167], v[20:23], v[100:103], 0
	v_mfma_f32_16x16x32_bf16 v[132:135], v[28:31], v[92:95], 0
	v_mfma_f32_16x16x32_bf16 v[168:171], v[28:31], v[100:103], 0
	v_mfma_f32_16x16x32_bf16 v[136:139], v[36:39], v[92:95], 0
	v_mfma_f32_16x16x32_bf16 v[172:175], v[36:39], v[100:103], 0
	v_mfma_f32_16x16x32_bf16 v[128:131], v[24:27], v[96:99], v[128:131]
	v_mfma_f32_16x16x32_bf16 v[164:167], v[24:27], v[104:107], v[164:167]
	v_mfma_f32_16x16x32_bf16 v[132:135], v[32:35], v[96:99], v[132:135]
	v_mfma_f32_16x16x32_bf16 v[168:171], v[32:35], v[104:107], v[168:171]
	v_mfma_f32_16x16x32_bf16 v[136:139], v[40:43], v[96:99], v[136:139]
	v_mfma_f32_16x16x32_bf16 v[172:175], v[40:43], v[104:107], v[172:175]
	s_waitcnt lgkmcnt(0)
	v_mfma_f32_16x16x32_bf16 v[140:143], v[44:47], v[92:95], 0
	v_mfma_f32_16x16x32_bf16 v[176:179], v[44:47], v[100:103], 0
	v_mfma_f32_16x16x32_bf16 v[180:183], v[216:219], v[100:103], 0
	v_mfma_f32_16x16x32_bf16 v[140:143], v[48:51], v[96:99], v[140:143]
	v_mfma_f32_16x16x32_bf16 v[176:179], v[48:51], v[104:107], v[176:179]
	v_mfma_f32_16x16x32_bf16 v[180:183], v[220:223], v[104:107], v[180:183]
	s_cmpk_gt_u32 s39, 0x3ff
	s_cbranch_scc1 .Lat_nopfk
	s_and_b32 s3, s39, 3
	s_bfe_u32 s4, s39, 0x70002
	s_lshr_b32 s5, s39, 9
	s_lshl_b32 s6, s5, 14
	s_lshl_b32 s7, s4, 7
	s_add_i32 s6, s6, s7
	s_sub_i32 s6, s6, 0x80
	s_mul_i32 s7, s6, 0x1400
	s_ashr_i32 s9, s7, 31
	s_add_u32 s40, s14, s7
	s_addc_u32 s41, s15, s9
	s_lshl_b32 s7, s3, 7
	s_add_u32 s40, s40, s7
	s_addc_u32 s41, s41, 0
	s_lshl_b32 s6, s5, 2
	s_add_i32 s6, s6, s3
	s_lshl_b32 s6, s6, 21
	s_lshl_b32 s7, s4, 8
	s_sub_i32 s7, s7, 0x100
	s_add_i32 s6, s6, s7
	s_ashr_i32 s7, s6, 31
	s_add_u32 s42, s16, s6
	s_addc_u32 s43, s17, s7
	global_load_dwordx4 v[92:95], v6, s[40:41] offset:0
	global_load_dwordx4 v[96:99], v6, s[40:41] offset:16
	global_load_dwordx4 v[100:103], v6, s[40:41] offset:32
	global_load_dwordx4 v[104:107], v6, s[40:41] offset:48

.Lat_nopfv:
	s_waitcnt lgkmcnt(2)
	v_mfma_f32_16x16x32_bf16 v[184:187], v[20:23], v[108:111], 0
	v_mfma_f32_16x16x32_bf16 v[188:191], v[24:27], v[108:111], 0
	v_mfma_f32_16x16x32_bf16 v[192:195], v[28:31], v[108:111], 0
	v_mfma_f32_16x16x32_bf16 v[196:199], v[32:35], v[108:111], 0
	v_mfma_f32_16x16x32_bf16 v[200:203], v[20:23], v[144:147], 0
	v_mfma_f32_16x16x32_bf16 v[204:207], v[24:27], v[144:147], 0
	v_mfma_f32_16x16x32_bf16 v[208:211], v[28:31], v[144:147], 0
	v_mfma_f32_16x16x32_bf16 v[212:215], v[32:35], v[144:147], 0
	ds_read2_b64 v[20:23], v11 offset0:40 offset1:44
	ds_read2_b64 v[24:27], v12 offset0:40 offset1:44
	ds_read2_b64 v[28:31], v13 offset0:40 offset1:44
	ds_read2_b64 v[32:35], v14 offset0:40 offset1:44
	v_mfma_f32_16x16x32_bf16 v[184:187], v[36:39], v[116:119], v[184:187]
	v_mfma_f32_16x16x32_bf16 v[188:191], v[40:43], v[116:119], v[188:191]
	v_mfma_f32_16x16x32_bf16 v[192:195], v[44:47], v[116:119], v[192:195]
	v_mfma_f32_16x16x32_bf16 v[196:199], v[48:51], v[116:119], v[196:199]
	v_mfma_f32_16x16x32_bf16 v[200:203], v[36:39], v[152:155], v[200:203]
	v_mfma_f32_16x16x32_bf16 v[204:207], v[40:43], v[152:155], v[204:207]
	v_mfma_f32_16x16x32_bf16 v[208:211], v[44:47], v[152:155], v[208:211]
	v_mfma_f32_16x16x32_bf16 v[212:215], v[48:51], v[152:155], v[212:215]
	ds_read2_b64 v[36:39], v11 offset0:48 offset1:52
	ds_read2_b64 v[40:43], v12 offset0:48 offset1:52
	ds_read2_b64 v[44:47], v13 offset0:48 offset1:52
	ds_read2_b64 v[48:51], v14 offset0:48 offset1:52
	s_waitcnt lgkmcnt(8)
	v_add_f32_e32 v232, v232, v233
	v_add_f32_e32 v226, v226, v227
	s_nop 0
	ds_bpermute_b32 v233, v16, v232
	ds_bpermute_b32 v227, v16, v226
	s_waitcnt lgkmcnt(6)
	v_mfma_f32_16x16x32_bf16 v[184:187], v[20:23], v[124:127], v[184:187]
	v_mfma_f32_16x16x32_bf16 v[188:191], v[24:27], v[124:127], v[188:191]
	v_mfma_f32_16x16x32_bf16 v[192:195], v[28:31], v[124:127], v[192:195]
	v_mfma_f32_16x16x32_bf16 v[196:199], v[32:35], v[124:127], v[196:199]
	v_mfma_f32_16x16x32_bf16 v[200:203], v[20:23], v[160:163], v[200:203]
	v_mfma_f32_16x16x32_bf16 v[204:207], v[24:27], v[160:163], v[204:207]
	v_mfma_f32_16x16x32_bf16 v[208:211], v[28:31], v[160:163], v[208:211]
	v_mfma_f32_16x16x32_bf16 v[212:215], v[32:35], v[160:163], v[212:215]
	ds_read2_b64 v[20:23], v11 offset0:56 offset1:60
	ds_read2_b64 v[24:27], v12 offset0:56 offset1:60
	ds_read2_b64 v[28:31], v13 offset0:56 offset1:60
	ds_read2_b64 v[32:35], v14 offset0:56 offset1:60
	s_waitcnt lgkmcnt(6)
	v_mfma_f32_16x16x32_bf16 v[184:187], v[36:39], v[132:135], v[184:187]
	v_mfma_f32_16x16x32_bf16 v[188:191], v[40:43], v[132:135], v[188:191]
	v_mfma_f32_16x16x32_bf16 v[192:195], v[44:47], v[132:135], v[192:195]
	v_mfma_f32_16x16x32_bf16 v[196:199], v[48:51], v[132:135], v[196:199]
	v_mfma_f32_16x16x32_bf16 v[200:203], v[36:39], v[168:171], v[200:203]
	v_mfma_f32_16x16x32_bf16 v[204:207], v[40:43], v[168:171], v[204:207]
	v_mfma_f32_16x16x32_bf16 v[208:211], v[44:47], v[168:171], v[208:211]
	v_mfma_f32_16x16x32_bf16 v[212:215], v[48:51], v[168:171], v[212:215]
	s_waitcnt lgkmcnt(0)
	v_mfma_f32_16x16x32_bf16 v[184:187], v[20:23], v[140:143], v[184:187]
	v_mfma_f32_16x16x32_bf16 v[188:191], v[24:27], v[140:143], v[188:191]
	v_mfma_f32_16x16x32_bf16 v[192:195], v[28:31], v[140:143], v[192:195]
	v_mfma_f32_16x16x32_bf16 v[196:199], v[32:35], v[140:143], v[196:199]
	v_mfma_f32_16x16x32_bf16 v[200:203], v[20:23], v[176:179], v[200:203]
	v_mfma_f32_16x16x32_bf16 v[204:207], v[24:27], v[176:179], v[204:207]
	v_mfma_f32_16x16x32_bf16 v[208:211], v[28:31], v[176:179], v[208:211]
	v_mfma_f32_16x16x32_bf16 v[212:215], v[32:35], v[176:179], v[212:215]
	v_add_f32_e32 v232, v232, v233
	v_add_f32_e32 v226, v226, v227
	v_add_f32_e32 v232, v232, v88
	v_add_f32_e32 v226, v226, v88
	v_rcp_f32_e32 v236, v232
	v_rcp_f32_e32 v230, v226
	v_mov_b32_e32 v237, v236
	v_mov_b32_e32 v231, v230
	s_nop 1
	v_pk_mul_f32 v[184:185], v[184:185], v[236:237]
	v_pk_mul_f32 v[186:187], v[186:187], v[236:237]
	v_pk_mul_f32 v[188:189], v[188:189], v[236:237]
	v_pk_mul_f32 v[190:191], v[190:191], v[236:237]
	v_pk_mul_f32 v[192:193], v[192:193], v[236:237]
	v_pk_mul_f32 v[194:195], v[194:195], v[236:237]
	v_pk_mul_f32 v[196:197], v[196:197], v[236:237]
	v_pk_mul_f32 v[198:199], v[198:199], v[236:237]
	v_pk_mul_f32 v[200:201], v[200:201], v[230:231]
	v_pk_mul_f32 v[202:203], v[202:203], v[230:231]
	v_pk_mul_f32 v[204:205], v[204:205], v[230:231]
	v_pk_mul_f32 v[206:207], v[206:207], v[230:231]
	v_pk_mul_f32 v[208:209], v[208:209], v[230:231]
	v_pk_mul_f32 v[210:211], v[210:211], v[230:231]
	v_pk_mul_f32 v[212:213], v[212:213], v[230:231]
	v_pk_mul_f32 v[214:215], v[214:215], v[230:231]
	v_cvt_pk_bf16_f32 v184, v184, v185
	v_cvt_pk_bf16_f32 v185, v186, v187
	v_cvt_pk_bf16_f32 v186, v188, v189
	v_cvt_pk_bf16_f32 v187, v190, v191
	v_cvt_pk_bf16_f32 v192, v192, v193
	v_cvt_pk_bf16_f32 v193, v194, v195
	v_cvt_pk_bf16_f32 v194, v196, v197
	v_cvt_pk_bf16_f32 v195, v198, v199
	v_cvt_pk_bf16_f32 v200, v200, v201
	v_cvt_pk_bf16_f32 v201, v202, v203
	v_cvt_pk_bf16_f32 v202, v204, v205
	v_cvt_pk_bf16_f32 v203, v206, v207
	v_cvt_pk_bf16_f32 v208, v208, v209
	v_cvt_pk_bf16_f32 v209, v210, v211
	v_cvt_pk_bf16_f32 v210, v212, v213
	v_cvt_pk_bf16_f32 v211, v214, v215
	s_nop 1
	v_permlane16_swap_b32 v184, v186
	v_permlane16_swap_b32 v185, v187
	v_permlane16_swap_b32 v192, v194
	v_permlane16_swap_b32 v193, v195
	v_permlane16_swap_b32 v200, v202
	v_permlane16_swap_b32 v201, v203
	v_permlane16_swap_b32 v208, v210
	v_permlane16_swap_b32 v209, v211
	global_store_dwordx4 v91, v[184:187], s[50:51]
	global_store_dwordx4 v91, v[192:195], s[50:51] offset:64
	global_store_dwordx4 v91, v[200:203], s[60:61]
	global_store_dwordx4 v91, v[208:211], s[60:61] offset:64
	s_mov_b32 s34, s39
	s_cmpk_gt_u32 s34, 0x3ff
	s_cbranch_scc0 .Lat_item
